# MLA LDS-read reschedule with pairwise waitcnts + conflict-free K swizzle + unscaled fp8 MFMA (MoBA blocks left as compiled)
# speedup vs baseline: 1.0071x; 1.0011x over previous
; template <int DQK, int KB>
; __device__ __forceinline__ void qkt(f32x16& p0, f32x16& p1, const char* K_lds, int r32, int hi, const bf16x8* qr) {
;     constexpr int ROWB = DQK * 2, SHM_K = 64 * ROWB;
;     p0 = f32x16{}; p1 = f32x16{};
;     const char* kb[4];
; #pragma unroll
;     for (int dd = 0; dd < 4; ++dd) kb[dd] = K_lds + KB * SHM_K + r32 * ROWB + (((dd * 16 + hi * 8) * 2) ^ ((r32 & 7) << 4));
; #pragma unroll
;     for (int d0 = 0; d0 < DQK / 16; ++d0) { const char* a = kb[d0 & 3] + (d0 >> 2) * 128;
;         bf16x8 b0 = *reinterpret_cast<const bf16x8*>(a);
;         bf16x8 b1 = *reinterpret_cast<const bf16x8*>(a + 32 * ROWB);
;         p0 = __builtin_amdgcn_mfma_f32_32x32x16_bf16(b0, qr[d0], p0, 0, 0, 0);
;         p1 = __builtin_amdgcn_mfma_f32_32x32x16_bf16(b1, qr[d0], p1, 0, 0, 0); }
; __device__ __forceinline__ void p4_moba_loop(Frame& F, const Args& A, const int qo, const bool cvmode) {
;     ...
;             { const bf16_t* qp = WSP(bf16_t, WS_P) + (size_t)(b * SEQ + pos) * NPROJ + h * 128 + hi * 8;
; #pragma unroll
;               for (int d0 = 0; d0 < 8; ++d0) qr[d0] = *(const bf16x8*)(qp + d0 * 16); }
;             const int ntile = own ? (tk >> 1) + 1 : 4;
;             const int qrel = pos - n * 256;
;             f32x16 o[4]; float m_reg = -1e30f, l_reg = 0.f;
; #pragma unroll
;             for (int d = 0; d < 4; ++d) o[d] = f32x16{};
.LBB0_548:
	s_or_b64 exec, exec, s[8:9]
	v_readlane_b32 s8, v255, 18
	v_subrev_u32_e32 v132, s77, v134
	s_nop 0
	v_add_u32_e32 v2, s8, v134
	s_movk_i32 s8, 0x2200
	v_mad_i64_i32 v[2:3], s[8:9], v2, s8, v[140:141]
	global_load_dwordx4 v[126:129], v[2:3], off
	global_load_dwordx4 v[122:125], v[2:3], off offset:32
	global_load_dwordx4 v[118:121], v[2:3], off offset:64
	global_load_dwordx4 v[114:117], v[2:3], off offset:96
	global_load_dwordx4 v[110:113], v[2:3], off offset:128
	global_load_dwordx4 v[106:109], v[2:3], off offset:160
	global_load_dwordx4 v[102:105], v[2:3], off offset:192
	global_load_dwordx4 v[98:101], v[2:3], off offset:224
	ds_read_b128 v[2:5], v166
	ds_read_b128 v[6:9], v166 offset:8192
	ds_read_b128 v[34:37], v167
	ds_read_b128 v[38:41], v167 offset:8192
	s_cmp_gt_u32 s80, 1
	s_waitcnt vmcnt(7) lgkmcnt(3)
	v_mfma_f32_32x32x16_bf16 v[18:33], v[2:5], v[126:129], 0
	s_waitcnt lgkmcnt(2)
	v_mfma_f32_32x32x16_bf16 v[2:17], v[6:9], v[126:129], 0
	s_waitcnt vmcnt(6) lgkmcnt(1)
	v_mfma_f32_32x32x16_bf16 v[18:33], v[34:37], v[122:125], v[18:33]
	s_waitcnt lgkmcnt(0)
	v_mfma_f32_32x32x16_bf16 v[2:17], v[38:41], v[122:125], v[2:17]
	ds_read_b128 v[34:37], v168
	ds_read_b128 v[38:41], v168 offset:8192
	s_waitcnt vmcnt(5) lgkmcnt(1)
	v_mfma_f32_32x32x16_bf16 v[18:33], v[34:37], v[118:121], v[18:33]
	s_waitcnt lgkmcnt(0)
	v_mfma_f32_32x32x16_bf16 v[2:17], v[38:41], v[118:121], v[2:17]
	ds_read_b128 v[34:37], v169
	ds_read_b128 v[38:41], v169 offset:8192
	s_waitcnt vmcnt(4) lgkmcnt(1)
	v_mfma_f32_32x32x16_bf16 v[18:33], v[34:37], v[114:117], v[18:33]
	s_waitcnt lgkmcnt(0)
	v_mfma_f32_32x32x16_bf16 v[2:17], v[38:41], v[114:117], v[2:17]
	ds_read_b128 v[34:37], v166 offset:128
	ds_read_b128 v[38:41], v166 offset:8320
	s_waitcnt vmcnt(3) lgkmcnt(1)
	v_mfma_f32_32x32x16_bf16 v[18:33], v[34:37], v[110:113], v[18:33]
	s_waitcnt lgkmcnt(0)
	v_mfma_f32_32x32x16_bf16 v[2:17], v[38:41], v[110:113], v[2:17]
	ds_read_b128 v[34:37], v167 offset:128
	ds_read_b128 v[38:41], v167 offset:8320
	s_waitcnt vmcnt(2) lgkmcnt(1)
	v_mfma_f32_32x32x16_bf16 v[18:33], v[34:37], v[106:109], v[18:33]
	s_waitcnt lgkmcnt(0)
	v_mfma_f32_32x32x16_bf16 v[2:17], v[38:41], v[106:109], v[2:17]
	ds_read_b128 v[34:37], v168 offset:128
	ds_read_b128 v[38:41], v168 offset:8320
	s_waitcnt vmcnt(1) lgkmcnt(1)
	v_mfma_f32_32x32x16_bf16 v[18:33], v[34:37], v[102:105], v[18:33]
	s_waitcnt lgkmcnt(0)
	v_mfma_f32_32x32x16_bf16 v[2:17], v[38:41], v[102:105], v[2:17]
	ds_read_b128 v[34:37], v169 offset:128
	ds_read_b128 v[38:41], v169 offset:8320
	s_waitcnt vmcnt(0) lgkmcnt(1)
	v_mfma_f32_32x32x16_bf16 v[18:33], v[34:37], v[98:101], v[18:33]
	v_mov_b32_e32 v34, v151
	s_nop 0
	v_mul_f32_e32 v36, v34, v155
	v_fma_f32 v42, v34, s34, v36
	v_fma_f32 v43, v34, s35, v36
	v_fma_f32 v44, v34, s2, v36
	v_fma_f32 v45, v34, s3, v36
	v_pk_fma_f32 v[46:47], v[34:35], s[36:37], v[36:37] op_sel_hi:[0,1,0]
	s_waitcnt lgkmcnt(0)
	v_mfma_f32_32x32x16_bf16 v[2:17], v[38:41], v[98:101], v[2:17]
	v_mov_b32_e32 v41, v34
	v_mul_f32_e32 v38, 0x42000000, v34
	v_fma_f32 v40, 0, v34, v36
	v_fmac_f32_e32 v41, v41, v155
	v_fma_f32 v48, v34, s38, v36
	v_fma_f32 v49, v34, s39, v36
	v_pk_fma_f32 v[50:51], v[34:35], s[40:41], v[36:37] op_sel_hi:[0,1,0]
	v_pk_fma_f32 v[52:53], v[34:35], s[42:43], v[36:37] op_sel_hi:[0,1,0]
	v_pk_fma_f32 v[34:35], v[34:35], s[44:45], v[36:37] op_sel_hi:[0,1,0]
	v_pk_add_f32 v[32:33], v[32:33], v[34:35]
	v_pk_add_f32 v[28:29], v[28:29], v[50:51]
	v_pk_add_f32 v[26:27], v[26:27], v[48:49]
	v_pk_add_f32 v[24:25], v[24:25], v[46:47]
	v_pk_add_f32 v[22:23], v[22:23], v[44:45]
	v_pk_add_f32 v[20:21], v[20:21], v[42:43]
	v_pk_add_f32 v[54:55], v[38:39], v[42:43] op_sel_hi:[0,1]
	v_pk_add_f32 v[44:45], v[38:39], v[44:45] op_sel_hi:[0,1]
	v_pk_add_f32 v[42:43], v[38:39], v[46:47] op_sel_hi:[0,1]
	v_pk_add_f32 v[46:47], v[38:39], v[48:49] op_sel_hi:[0,1]
	v_pk_add_f32 v[48:49], v[38:39], v[50:51] op_sel_hi:[0,1]
	v_pk_add_f32 v[36:37], v[38:39], v[52:53] op_sel_hi:[0,1]
	v_pk_add_f32 v[34:35], v[38:39], v[34:35] op_sel_hi:[0,1]
	v_pk_add_f32 v[50:51], v[38:39], v[40:41] op_sel_hi:[0,1]
	v_pk_add_f32 v[30:31], v[30:31], v[52:53]
	v_pk_add_f32 v[18:19], v[18:19], v[40:41]
	v_pk_add_f32 v[34:35], v[16:17], v[34:35]
	v_pk_add_f32 v[36:37], v[14:15], v[36:37]
	v_pk_add_f32 v[38:39], v[12:13], v[48:49]
	v_pk_add_f32 v[40:41], v[10:11], v[46:47]
	v_pk_add_f32 v[42:43], v[8:9], v[42:43]
	v_pk_add_f32 v[44:45], v[6:7], v[44:45]
	v_pk_add_f32 v[46:47], v[4:5], v[54:55]
	v_pk_add_f32 v[48:49], v[2:3], v[50:51]
	s_cbranch_scc1 .LBB0_550
; __device__ __forceinline__ void mask_tile(f32x16& p0, f32x16& p1, int dq) {
;     const float NEG = -__builtin_inff();
; #pragma unroll
;     for (int r = 0; r < 16; ++r) {
;         const int c = (r & 3) + 8 * (r >> 2);
;         if (dq - c < 0) p0[r] = NEG;
;         if (dq - c - 32 < 0) p1[r] = NEG;
;     }
; }
	v_sub_u32_e32 v2, v132, v154
	v_cmp_gt_i32_e64 s[66:67], 26, v2
	v_cmp_gt_i32_e64 s[68:69], 27, v2
	v_cmp_gt_i32_e64 s[64:65], 25, v2
	s_and_b64 s[66:67], s[68:69], s[66:67]
	v_cmp_gt_i32_e64 s[62:63], 24, v2
	s_and_b64 s[64:65], s[66:67], s[64:65]
	v_cmp_gt_i32_e64 s[60:61], 19, v2
	s_and_b64 s[62:63], s[64:65], s[62:63]
	v_cmp_gt_i32_e64 s[58:59], 18, v2
	s_and_b64 s[60:61], s[62:63], s[60:61]
	v_cmp_gt_i32_e64 s[56:57], 17, v2
	s_and_b64 s[58:59], s[60:61], s[58:59]
	v_cmp_gt_i32_e64 s[54:55], 16, v2
	s_and_b64 s[56:57], s[58:59], s[56:57]
	v_cmp_gt_i32_e64 s[52:53], 11, v2
	s_and_b64 s[54:55], s[56:57], s[54:55]
	v_cmp_gt_i32_e64 s[50:51], 10, v2
	s_and_b64 s[52:53], s[54:55], s[52:53]
	v_cmp_gt_i32_e64 s[48:49], 9, v2
	s_and_b64 s[50:51], s[52:53], s[50:51]
	v_cmp_gt_i32_e64 s[46:47], 8, v2
	s_and_b64 s[48:49], s[50:51], s[48:49]
	v_cmp_gt_i32_e64 s[44:45], 3, v2
	s_and_b64 s[46:47], s[48:49], s[46:47]
	v_cmp_gt_i32_e64 s[42:43], 2, v2
	s_and_b64 s[44:45], s[46:47], s[44:45]
	v_cmp_gt_i32_e64 s[40:41], 1, v2
	s_and_b64 s[42:43], s[44:45], s[42:43]
	v_cmp_gt_i32_e64 s[38:39], 0, v2
	s_and_b64 s[40:41], s[42:43], s[40:41]
	s_and_b64 s[38:39], s[40:41], s[38:39]
	v_cmp_gt_i32_e64 s[36:37], 58, v2
	v_cndmask_b32_e64 v18, v18, v147, s[38:39]
	v_cmp_gt_i32_e64 s[38:39], 59, v2
	v_cmp_gt_i32_e64 s[34:35], 57, v2
	s_and_b64 s[36:37], s[38:39], s[36:37]
	v_cmp_gt_i32_e64 s[30:31], 56, v2
	s_and_b64 s[34:35], s[36:37], s[34:35]
	v_cmp_gt_i32_e64 s[28:29], 51, v2
	s_and_b64 s[30:31], s[34:35], s[30:31]
	v_cmp_gt_i32_e64 s[26:27], 50, v2
	s_and_b64 s[28:29], s[30:31], s[28:29]
	v_cmp_gt_i32_e64 s[24:25], 49, v2
	s_and_b64 s[26:27], s[28:29], s[26:27]
	v_cmp_gt_i32_e64 s[22:23], 48, v2
	s_and_b64 s[24:25], s[26:27], s[24:25]
	v_cmp_gt_i32_e64 s[20:21], 43, v2
	s_and_b64 s[22:23], s[24:25], s[22:23]
	v_cmp_gt_i32_e64 s[18:19], 42, v2
	s_and_b64 s[20:21], s[22:23], s[20:21]
	v_cmp_gt_i32_e64 s[16:17], 41, v2
	s_and_b64 s[18:19], s[20:21], s[18:19]
	v_cmp_gt_i32_e64 s[14:15], 40, v2
	s_and_b64 s[16:17], s[18:19], s[16:17]
	v_cmp_gt_i32_e64 s[12:13], 35, v2
	s_and_b64 s[14:15], s[16:17], s[14:15]
	v_cmp_gt_i32_e64 s[10:11], 34, v2
	s_and_b64 s[12:13], s[14:15], s[12:13]
	v_cmp_gt_i32_e64 s[8:9], 33, v2
	s_and_b64 s[10:11], s[12:13], s[10:11]
	v_cmp_gt_i32_e32 vcc, 32, v2
	s_and_b64 s[8:9], s[10:11], s[8:9]
	v_cndmask_b32_e64 v21, v21, v147, s[44:45]
	s_mov_b32 s44, 0x41d00000
	v_cndmask_b32_e64 v20, v20, v147, s[42:43]
	s_mov_b32 s42, 0x41c00000
	v_cndmask_b32_e64 v19, v19, v147, s[40:41]
	s_mov_b32 s40, 0x41900000
	v_cndmask_b32_e64 v35, v35, v147, s[38:39]
	s_mov_b32 s38, 0x41800000
	v_cndmask_b32_e64 v34, v34, v147, s[36:37]
	s_mov_b32 s36, 0x41200000
	v_cndmask_b32_e64 v37, v37, v147, s[34:35]
	s_mov_b32 s34, 2.0
	s_and_b64 vcc, s[8:9], vcc
	v_cndmask_b32_e64 v33, v33, v147, s[68:69]
	v_cndmask_b32_e64 v32, v32, v147, s[66:67]
	v_cndmask_b32_e64 v31, v31, v147, s[64:65]
	v_cndmask_b32_e64 v30, v30, v147, s[62:63]
	v_cndmask_b32_e64 v29, v29, v147, s[60:61]
	v_cndmask_b32_e64 v28, v28, v147, s[58:59]
	v_cndmask_b32_e64 v27, v27, v147, s[56:57]
	v_cndmask_b32_e64 v26, v26, v147, s[54:55]
	v_cndmask_b32_e64 v25, v25, v147, s[52:53]
	v_cndmask_b32_e64 v24, v24, v147, s[50:51]
	v_cndmask_b32_e64 v23, v23, v147, s[48:49]
	v_cndmask_b32_e64 v22, v22, v147, s[46:47]
	s_mov_b32 s45, 0x41d80000
	s_mov_b32 s43, 0x41c80000
	s_mov_b32 s41, 0x41980000
	s_mov_b32 s39, 0x41880000
	s_mov_b32 s37, 0x41300000
	s_mov_b32 s35, 0x40400000
	v_cndmask_b32_e64 v36, v36, v147, s[30:31]
	v_cndmask_b32_e64 v39, v39, v147, s[28:29]
	v_cndmask_b32_e64 v38, v38, v147, s[26:27]
	v_cndmask_b32_e64 v41, v41, v147, s[24:25]
	v_cndmask_b32_e64 v40, v40, v147, s[22:23]
	v_cndmask_b32_e64 v43, v43, v147, s[20:21]
	v_cndmask_b32_e64 v42, v42, v147, s[18:19]
	v_cndmask_b32_e64 v45, v45, v147, s[16:17]
	v_cndmask_b32_e64 v44, v44, v147, s[14:15]
	v_cndmask_b32_e64 v47, v47, v147, s[12:13]
	v_cndmask_b32_e64 v46, v46, v147, s[10:11]
	v_cndmask_b32_e64 v49, v49, v147, s[8:9]
	v_cndmask_b32_e32 v48, v48, v147, vcc

; template <int DQK> __device__ __forceinline__ void partialSM(f32x16& p0, f32x16& p1, float& m_reg, float& mn, float& alpha) {
;     ...
;     const float mnL = -mn * C2;
; #pragma unroll
;     for (int r = 0; r < 16; ++r) p0[r] = fmaf(p0[r], C2, mnL);
; #pragma unroll
;     for (int r = 0; r < 16; ++r) p1[r] = fmaf(p1[r], C2, mnL);
; #pragma unroll
;     for (int r = 0; r < 16; ++r) p0[r] = __builtin_amdgcn_exp2f(p0[r]);
; }
; __device__ __forceinline__ void finishSM(f32x16& p0, f32x16& p1, float alpha, float& l_reg, bf16x8& pa0, bf16x8& pa1, bf16x8& pa2, bf16x8& pa3) {
; #pragma unroll
;     for (int r = 0; r < 16; ++r) p1[r] = __builtin_amdgcn_exp2f(p1[r]);
;     float ps = 0;
; #pragma unroll
;     for (int r = 0; r < 16; ++r) ps += p0[r];
; #pragma unroll
;     for (int r = 0; r < 16; ++r) ps += p1[r];
;     { auto rr = __builtin_amdgcn_permlane32_swap(__float_as_uint(ps), __float_as_uint(ps), false, false);
;       ps = __uint_as_float(rr[0]) + __uint_as_float(rr[1]); }
;     l_reg = l_reg * alpha + ps;
;     ...
;     PK4(p0, 0, pa0); PK4(p0, 8, pa1); PK4(p1, 0, pa2); PK4(p1, 8, pa3);
; template <int VB>
; __device__ __forceinline__ void pv_tile(f32x16* o, int vb0, bf16x8 pa0, bf16x8 pa1, bf16x8 pa2, bf16x8 pa3) {
;     ...
;     PV_D0(0); PV_D0(1); PV_D0(2); PV_D0(3);
.LBB0_559:
	v_cndmask_b32_e64 v137, v148, v51, s[8:9]
	v_mul_f32_e32 v51, 0xbe0293ee, v137
	v_fmamk_f32 v18, v18, 0x3e0293ee, v51
	v_fmamk_f32 v19, v19, 0x3e0293ee, v51
	v_exp_f32_e32 v18, v18
	v_fmamk_f32 v20, v20, 0x3e0293ee, v51
	v_exp_f32_e32 v19, v19
	v_fmamk_f32 v21, v21, 0x3e0293ee, v51
	v_exp_f32_e32 v20, v20
	v_fmamk_f32 v22, v22, 0x3e0293ee, v51
	v_fmamk_f32 v23, v23, 0x3e0293ee, v51
	v_fmamk_f32 v24, v24, 0x3e0293ee, v51
	v_fmamk_f32 v25, v25, 0x3e0293ee, v51
	v_fmamk_f32 v26, v26, 0x3e0293ee, v51
	v_fmamk_f32 v27, v27, 0x3e0293ee, v51
	v_fmamk_f32 v28, v28, 0x3e0293ee, v51
	v_fmamk_f32 v29, v29, 0x3e0293ee, v51
	v_fmamk_f32 v30, v30, 0x3e0293ee, v51
	v_fmamk_f32 v31, v31, 0x3e0293ee, v51
	v_fmamk_f32 v32, v32, 0x3e0293ee, v51
	v_fmamk_f32 v33, v33, 0x3e0293ee, v51
	v_fmamk_f32 v48, v48, 0x3e0293ee, v51
	v_fmamk_f32 v49, v49, 0x3e0293ee, v51
	v_fmamk_f32 v46, v46, 0x3e0293ee, v51
	v_fmamk_f32 v47, v47, 0x3e0293ee, v51
	v_fmamk_f32 v44, v44, 0x3e0293ee, v51
	v_fmamk_f32 v45, v45, 0x3e0293ee, v51
	v_fmamk_f32 v42, v42, 0x3e0293ee, v51
	v_fmamk_f32 v43, v43, 0x3e0293ee, v51
	v_fmamk_f32 v40, v40, 0x3e0293ee, v51
	v_fmamk_f32 v41, v41, 0x3e0293ee, v51
	v_fmamk_f32 v38, v38, 0x3e0293ee, v51
	v_fmamk_f32 v39, v39, 0x3e0293ee, v51
	v_fmamk_f32 v36, v36, 0x3e0293ee, v51
	v_fmamk_f32 v37, v37, 0x3e0293ee, v51
	v_fmamk_f32 v34, v34, 0x3e0293ee, v51
	v_fmac_f32_e32 v51, 0x3e0293ee, v35
	v_exp_f32_e32 v21, v21
	v_exp_f32_e32 v22, v22
	v_exp_f32_e32 v35, v48
	v_exp_f32_e32 v48, v49
	v_exp_f32_e32 v49, v51
	v_add_f32_e32 v51, 0, v18
	v_exp_f32_e32 v23, v23
	v_add_f32_e32 v51, v19, v51
	v_exp_f32_e32 v24, v24
	v_add_f32_e32 v51, v20, v51
	v_exp_f32_e32 v25, v25
	v_add_f32_e32 v51, v21, v51
	v_exp_f32_e32 v26, v26
	v_add_f32_e32 v51, v22, v51
	v_exp_f32_e32 v27, v27
	v_add_f32_e32 v51, v23, v51
	v_exp_f32_e32 v28, v28
	v_add_f32_e32 v51, v24, v51
	v_exp_f32_e32 v29, v29
	v_add_f32_e32 v51, v25, v51
	v_exp_f32_e32 v30, v30
	v_add_f32_e32 v51, v26, v51
	v_exp_f32_e32 v31, v31
	v_add_f32_e32 v51, v27, v51
	v_exp_f32_e32 v32, v32
	v_add_f32_e32 v51, v28, v51
	v_exp_f32_e32 v33, v33
	v_add_f32_e32 v51, v29, v51
	v_add_f32_e32 v51, v30, v51
	v_add_f32_e32 v51, v31, v51
	v_exp_f32_e32 v46, v46
	v_add_f32_e32 v51, v32, v51
	v_exp_f32_e32 v47, v47
	v_add_f32_e32 v51, v33, v51
	v_exp_f32_e32 v44, v44
	v_add_f32_e32 v51, v35, v51
	v_exp_f32_e32 v45, v45
	v_add_f32_e32 v51, v48, v51
	v_exp_f32_e32 v42, v42
	v_add_f32_e32 v51, v46, v51
	v_exp_f32_e32 v43, v43
	v_add_f32_e32 v51, v47, v51
	v_exp_f32_e32 v40, v40
	v_add_f32_e32 v51, v44, v51
	v_exp_f32_e32 v41, v41
	v_add_f32_e32 v51, v45, v51
	v_exp_f32_e32 v38, v38
	v_add_f32_e32 v51, v42, v51
	v_exp_f32_e32 v39, v39
	v_add_f32_e32 v51, v43, v51
	v_exp_f32_e32 v36, v36
	v_add_f32_e32 v51, v40, v51
	v_exp_f32_e32 v37, v37
	v_add_f32_e32 v51, v41, v51
	v_exp_f32_e32 v34, v34
	v_add_f32_e32 v51, v38, v51
	v_add_f32_e32 v51, v39, v51
	v_add_f32_e32 v51, v36, v51
	v_add_f32_e32 v51, v37, v51
	v_add_f32_e32 v51, v34, v51
	v_add_f32_e32 v51, v49, v51
	v_mov_b32_e32 v52, v51
	s_nop 1
	v_permlane32_swap_b32_e32 v51, v52
	s_and_b64 s[8:9], s[74:75], exec
	v_add_f32_e32 v145, v51, v52
	s_cselect_b32 s33, s81, 4
	v_fmac_f32_e32 v145, 0, v50
	v_cvt_pk_bf16_f32 v66, v18, v19
	v_cvt_pk_bf16_f32 v67, v20, v21
	v_cvt_pk_bf16_f32 v68, v22, v23
	v_cvt_pk_bf16_f32 v69, v24, v25
	v_cvt_pk_bf16_f32 v70, v26, v27
	v_cvt_pk_bf16_f32 v71, v28, v29
	v_cvt_pk_bf16_f32 v72, v30, v31
	v_cvt_pk_bf16_f32 v73, v32, v33
	v_cvt_pk_bf16_f32 v74, v35, v48
	v_cvt_pk_bf16_f32 v75, v46, v47
	v_cvt_pk_bf16_f32 v76, v44, v45
	v_cvt_pk_bf16_f32 v77, v42, v43
	v_cvt_pk_bf16_f32 v78, v40, v41
	v_cvt_pk_bf16_f32 v79, v38, v39
	v_cvt_pk_bf16_f32 v80, v36, v37
	v_cvt_pk_bf16_f32 v81, v34, v49
	s_nop 0
	v_permlane32_swap_b32_e32 v66, v68
	v_permlane32_swap_b32_e32 v67, v69
	v_permlane32_swap_b32_e32 v70, v72
	v_permlane32_swap_b32_e32 v71, v73
	v_permlane32_swap_b32_e32 v74, v76
	v_permlane32_swap_b32_e32 v75, v77
	v_permlane32_swap_b32_e32 v78, v80
	v_permlane32_swap_b32_e32 v79, v81
	ds_read_b64_tr_b16 v[34:35], v152 offset:0
	ds_read_b64_tr_b16 v[36:37], v152 offset:0x800
	ds_read_b64_tr_b16 v[38:39], v152 offset:0x1000
	ds_read_b64_tr_b16 v[40:41], v152 offset:0x1800
	ds_read_b64_tr_b16 v[42:43], v152 offset:0x2000
	ds_read_b64_tr_b16 v[44:45], v152 offset:0x2800
	ds_read_b64_tr_b16 v[46:47], v152 offset:0x3000
	ds_read_b64_tr_b16 v[48:49], v152 offset:0x3800
	s_waitcnt lgkmcnt(0)
	s_nop 0
	v_mfma_f32_32x32x16_bf16 v[18:33], v[66:69], v[34:37], v[2:17]
	ds_read_b64_tr_b16 v[50:51], v152 offset:0x200
	ds_read_b64_tr_b16 v[52:53], v152 offset:0xa00
	ds_read_b64_tr_b16 v[54:55], v152 offset:0x1200
	ds_read_b64_tr_b16 v[56:57], v152 offset:0x1a00
	ds_read_b64_tr_b16 v[58:59], v152 offset:0x2200
	ds_read_b64_tr_b16 v[60:61], v152 offset:0x2a00
	ds_read_b64_tr_b16 v[62:63], v152 offset:0x3200
	v_mfma_f32_32x32x16_bf16 v[18:33], v[70:73], v[38:41], v[18:33]
	ds_read_b64_tr_b16 v[64:65], v152 offset:0x3a00
	s_waitcnt lgkmcnt(0)
	v_mfma_f32_32x32x16_bf16 v[18:33], v[74:77], v[42:45], v[18:33]
	v_mfma_f32_32x32x16_bf16 v[18:33], v[78:81], v[46:49], v[18:33]
	v_mfma_f32_32x32x16_bf16 v[34:49], v[66:69], v[50:53], v[2:17]
	ds_read_b64_tr_b16 v[82:83], v152 offset:0x400
	ds_read_b64_tr_b16 v[84:85], v152 offset:0xc00
	ds_read_b64_tr_b16 v[86:87], v152 offset:0x1400
	ds_read_b64_tr_b16 v[88:89], v152 offset:0x1c00
	ds_read_b64_tr_b16 v[90:91], v152 offset:0x2400
	ds_read_b64_tr_b16 v[92:93], v152 offset:0x2c00
	ds_read_b64_tr_b16 v[94:95], v152 offset:0x3400
	v_mfma_f32_32x32x16_bf16 v[34:49], v[70:73], v[54:57], v[34:49]
	ds_read_b64_tr_b16 v[96:97], v152 offset:0x3c00
	s_waitcnt lgkmcnt(0)
	v_mfma_f32_32x32x16_bf16 v[34:49], v[74:77], v[58:61], v[34:49]
	v_mfma_f32_32x32x16_bf16 v[34:49], v[78:81], v[62:65], v[34:49]
	v_mfma_f32_32x32x16_bf16 v[50:65], v[66:69], v[82:85], v[2:17]
	ds_read_b64_tr_b16 v[82:83], v152 offset:0x600
	ds_read_b64_tr_b16 v[84:85], v152 offset:0xe00
	v_mfma_f32_32x32x16_bf16 v[50:65], v[70:73], v[86:89], v[50:65]
	ds_read_b64_tr_b16 v[86:87], v152 offset:0x1600
	ds_read_b64_tr_b16 v[88:89], v152 offset:0x1e00
	v_mfma_f32_32x32x16_bf16 v[50:65], v[74:77], v[90:93], v[50:65]
	ds_read_b64_tr_b16 v[90:91], v152 offset:0x2600
	ds_read_b64_tr_b16 v[92:93], v152 offset:0x2e00
	v_mfma_f32_32x32x16_bf16 v[50:65], v[78:81], v[94:97], v[50:65]
	ds_read_b64_tr_b16 v[94:95], v152 offset:0x3600
	ds_read_b64_tr_b16 v[96:97], v152 offset:0x3e00
	s_waitcnt lgkmcnt(0)
	v_mfma_f32_32x32x16_bf16 v[2:17], v[66:69], v[82:85], v[2:17]
	s_cmp_lt_u32 s33, 2
	v_mfma_f32_32x32x16_bf16 v[2:17], v[70:73], v[86:89], v[2:17]
	v_mfma_f32_32x32x16_bf16 v[2:17], v[74:77], v[90:93], v[2:17]
	v_mfma_f32_32x32x16_bf16 v[2:17], v[78:81], v[94:97], v[2:17]
	s_cbranch_scc0 .LBB0_692
	s_cmp_lt_u32 s33, 3
	s_cbranch_scc0 .LBB0_699

; template <int DQK, int KB>
; __device__ __forceinline__ void qkt(f32x16& p0, f32x16& p1, const char* K_lds, int r32, int hi, const bf16x8* qr) {
;     constexpr int ROWB = DQK * 2, SHM_K = 64 * ROWB;
;     p0 = f32x16{}; p1 = f32x16{};
;     const char* kb[4];
; #pragma unroll
;     for (int dd = 0; dd < 4; ++dd) kb[dd] = K_lds + KB * SHM_K + r32 * ROWB + (((dd * 16 + hi * 8) * 2) ^ ((r32 & 7) << 4));
; #pragma unroll
;     for (int d0 = 0; d0 < DQK / 16; ++d0) { const char* a = kb[d0 & 3] + (d0 >> 2) * 128;
;         bf16x8 b0 = *reinterpret_cast<const bf16x8*>(a);
;         bf16x8 b1 = *reinterpret_cast<const bf16x8*>(a + 32 * ROWB);
;         p0 = __builtin_amdgcn_mfma_f32_32x32x16_bf16(b0, qr[d0], p0, 0, 0, 0);
;         p1 = __builtin_amdgcn_mfma_f32_32x32x16_bf16(b1, qr[d0], p1, 0, 0, 0); }
.LBB0_692:
	ds_read_b128 v[66:69], v166 offset:16384
	ds_read_b128 v[70:73], v166 offset:24576
	ds_read_b128 v[174:177], v167 offset:16384
	ds_read_b128 v[178:181], v167 offset:24576
	s_cmp_gt_u32 s80, 3
	s_waitcnt lgkmcnt(3)
	v_mfma_f32_32x32x16_bf16 v[82:97], v[66:69], v[126:129], 0
	s_waitcnt lgkmcnt(2)
	v_mfma_f32_32x32x16_bf16 v[66:81], v[70:73], v[126:129], 0
	s_waitcnt lgkmcnt(1)
	v_mfma_f32_32x32x16_bf16 v[82:97], v[174:177], v[122:125], v[82:97]
	s_waitcnt lgkmcnt(0)
	v_mfma_f32_32x32x16_bf16 v[66:81], v[178:181], v[122:125], v[66:81]
	ds_read_b128 v[174:177], v168 offset:16384
	ds_read_b128 v[178:181], v168 offset:24576
	s_waitcnt lgkmcnt(1)
	v_mfma_f32_32x32x16_bf16 v[82:97], v[174:177], v[118:121], v[82:97]
	s_waitcnt lgkmcnt(0)
	v_mfma_f32_32x32x16_bf16 v[66:81], v[178:181], v[118:121], v[66:81]
	ds_read_b128 v[174:177], v169 offset:16384
	ds_read_b128 v[178:181], v169 offset:24576
	s_waitcnt lgkmcnt(1)
	v_mfma_f32_32x32x16_bf16 v[82:97], v[174:177], v[114:117], v[82:97]
	s_waitcnt lgkmcnt(0)
	v_mfma_f32_32x32x16_bf16 v[66:81], v[178:181], v[114:117], v[66:81]
	ds_read_b128 v[174:177], v166 offset:16512
	ds_read_b128 v[178:181], v166 offset:24704
	s_waitcnt lgkmcnt(1)
	v_mfma_f32_32x32x16_bf16 v[82:97], v[174:177], v[110:113], v[82:97]
	s_waitcnt lgkmcnt(0)
	v_mfma_f32_32x32x16_bf16 v[66:81], v[178:181], v[110:113], v[66:81]
	ds_read_b128 v[174:177], v167 offset:16512
	ds_read_b128 v[178:181], v167 offset:24704
	s_waitcnt lgkmcnt(1)
	v_mfma_f32_32x32x16_bf16 v[82:97], v[174:177], v[106:109], v[82:97]
	s_waitcnt lgkmcnt(0)
	v_mfma_f32_32x32x16_bf16 v[66:81], v[178:181], v[106:109], v[66:81]
	ds_read_b128 v[174:177], v168 offset:16512
	ds_read_b128 v[178:181], v168 offset:24704
	s_waitcnt lgkmcnt(1)
	v_mfma_f32_32x32x16_bf16 v[82:97], v[174:177], v[102:105], v[82:97]
	s_waitcnt lgkmcnt(0)
	v_mfma_f32_32x32x16_bf16 v[66:81], v[178:181], v[102:105], v[66:81]
	ds_read_b128 v[174:177], v169 offset:16512
	ds_read_b128 v[178:181], v169 offset:24704
	s_waitcnt lgkmcnt(1)
	v_mfma_f32_32x32x16_bf16 v[82:97], v[174:177], v[98:101], v[82:97]
	v_mov_b32_e32 v174, v151
	s_nop 0
	v_mul_f32_e32 v176, v174, v157
	v_fma_f32 v182, v174, s34, v176
	v_fma_f32 v183, v174, s35, v176
	v_fma_f32 v184, v174, s2, v176
	v_fma_f32 v185, v174, s3, v176
	v_pk_fma_f32 v[186:187], v[174:175], s[36:37], v[176:177] op_sel_hi:[0,1,0]
	s_waitcnt lgkmcnt(0)
	v_mfma_f32_32x32x16_bf16 v[66:81], v[178:181], v[98:101], v[66:81]
	v_mov_b32_e32 v181, v174
	v_mul_f32_e32 v178, 0x42000000, v174
	v_fma_f32 v180, 0, v174, v176
	v_fmac_f32_e32 v181, v181, v157
	v_fma_f32 v188, v174, s38, v176
	v_fma_f32 v189, v174, s39, v176
	v_pk_fma_f32 v[190:191], v[174:175], s[40:41], v[176:177] op_sel_hi:[0,1,0]
	v_pk_fma_f32 v[192:193], v[174:175], s[42:43], v[176:177] op_sel_hi:[0,1,0]
	v_pk_fma_f32 v[174:175], v[174:175], s[44:45], v[176:177] op_sel_hi:[0,1,0]
	v_pk_add_f32 v[96:97], v[96:97], v[174:175]
	v_pk_add_f32 v[92:93], v[92:93], v[190:191]
	v_pk_add_f32 v[90:91], v[90:91], v[188:189]
	v_pk_add_f32 v[88:89], v[88:89], v[186:187]
	v_pk_add_f32 v[86:87], v[86:87], v[184:185]
	v_pk_add_f32 v[84:85], v[84:85], v[182:183]
	v_pk_add_f32 v[176:177], v[178:179], v[182:183] op_sel_hi:[0,1]
	v_pk_add_f32 v[182:183], v[178:179], v[184:185] op_sel_hi:[0,1]
	v_pk_add_f32 v[184:185], v[178:179], v[186:187] op_sel_hi:[0,1]
	v_pk_add_f32 v[186:187], v[178:179], v[188:189] op_sel_hi:[0,1]
	v_pk_add_f32 v[188:189], v[178:179], v[190:191] op_sel_hi:[0,1]
	v_pk_add_f32 v[190:191], v[178:179], v[192:193] op_sel_hi:[0,1]
	v_pk_add_f32 v[174:175], v[178:179], v[174:175] op_sel_hi:[0,1]
	v_pk_add_f32 v[178:179], v[178:179], v[180:181] op_sel_hi:[0,1]
	v_pk_add_f32 v[94:95], v[94:95], v[192:193]
	v_pk_add_f32 v[82:83], v[82:83], v[180:181]
	v_pk_add_f32 v[80:81], v[80:81], v[174:175]
	v_pk_add_f32 v[78:79], v[78:79], v[190:191]
	v_pk_add_f32 v[76:77], v[76:77], v[188:189]
	v_pk_add_f32 v[74:75], v[74:75], v[186:187]
	v_pk_add_f32 v[72:73], v[72:73], v[184:185]
	v_pk_add_f32 v[70:71], v[70:71], v[182:183]
	v_pk_add_f32 v[68:69], v[68:69], v[176:177]
	v_pk_add_f32 v[66:67], v[66:67], v[178:179]
	s_cbranch_scc1 .LBB0_694
; __device__ __forceinline__ void mask_tile(f32x16& p0, f32x16& p1, int dq) {
;     const float NEG = -__builtin_inff();
; #pragma unroll
;     for (int r = 0; r < 16; ++r) {
;         const int c = (r & 3) + 8 * (r >> 2);
;         if (dq - c < 0) p0[r] = NEG;
;         if (dq - c - 32 < 0) p1[r] = NEG;
;     }
; }
	v_sub_u32_e32 v171, v132, v154
	v_subrev_u32_e32 v171, 64, v171
	v_cmp_gt_i32_e64 s[66:67], 26, v171
	v_cmp_gt_i32_e64 s[68:69], 27, v171
	v_cmp_gt_i32_e64 s[64:65], 25, v171
	s_and_b64 s[66:67], s[68:69], s[66:67]
	v_cmp_gt_i32_e64 s[62:63], 24, v171
	s_and_b64 s[64:65], s[66:67], s[64:65]
	v_cmp_gt_i32_e64 s[60:61], 19, v171
	s_and_b64 s[62:63], s[64:65], s[62:63]
	v_cmp_gt_i32_e64 s[58:59], 18, v171
	s_and_b64 s[60:61], s[62:63], s[60:61]
	v_cmp_gt_i32_e64 s[56:57], 17, v171
	s_and_b64 s[58:59], s[60:61], s[58:59]
	v_cmp_gt_i32_e64 s[54:55], 16, v171
	s_and_b64 s[56:57], s[58:59], s[56:57]
	v_cmp_gt_i32_e64 s[52:53], 11, v171
	s_and_b64 s[54:55], s[56:57], s[54:55]
	v_cmp_gt_i32_e64 s[50:51], 10, v171
	s_and_b64 s[52:53], s[54:55], s[52:53]
	v_cmp_gt_i32_e64 s[48:49], 9, v171
	s_and_b64 s[50:51], s[52:53], s[50:51]
	v_cmp_gt_i32_e64 s[46:47], 8, v171
	s_and_b64 s[48:49], s[50:51], s[48:49]
	v_cmp_gt_i32_e64 s[44:45], 3, v171
	s_and_b64 s[46:47], s[48:49], s[46:47]
	v_cmp_gt_i32_e64 s[42:43], 2, v171
	s_and_b64 s[44:45], s[46:47], s[44:45]
	v_cmp_gt_i32_e64 s[40:41], 1, v171
	s_and_b64 s[42:43], s[44:45], s[42:43]
	v_cmp_gt_i32_e64 s[38:39], 0, v171
	s_and_b64 s[40:41], s[42:43], s[40:41]
	s_and_b64 s[38:39], s[40:41], s[38:39]
	v_cmp_gt_i32_e64 s[36:37], 58, v171
	v_cndmask_b32_e64 v82, v82, v147, s[38:39]
	v_cmp_gt_i32_e64 s[38:39], 59, v171
	v_cmp_gt_i32_e64 s[34:35], 57, v171
	s_and_b64 s[36:37], s[38:39], s[36:37]
	v_cmp_gt_i32_e64 s[30:31], 56, v171
	s_and_b64 s[34:35], s[36:37], s[34:35]
	v_cmp_gt_i32_e64 s[28:29], 51, v171
	s_and_b64 s[30:31], s[34:35], s[30:31]
	v_cmp_gt_i32_e64 s[26:27], 50, v171
	s_and_b64 s[28:29], s[30:31], s[28:29]
	v_cmp_gt_i32_e64 s[24:25], 49, v171
	s_and_b64 s[26:27], s[28:29], s[26:27]
	v_cmp_gt_i32_e64 s[22:23], 48, v171
	s_and_b64 s[24:25], s[26:27], s[24:25]
	v_cmp_gt_i32_e64 s[20:21], 43, v171
	s_and_b64 s[22:23], s[24:25], s[22:23]
	v_cmp_gt_i32_e64 s[18:19], 42, v171
	s_and_b64 s[20:21], s[22:23], s[20:21]
	v_cmp_gt_i32_e64 s[16:17], 41, v171
	s_and_b64 s[18:19], s[20:21], s[18:19]
	v_cmp_gt_i32_e64 s[14:15], 40, v171
	s_and_b64 s[16:17], s[18:19], s[16:17]
	v_cmp_gt_i32_e64 s[12:13], 35, v171
	s_and_b64 s[14:15], s[16:17], s[14:15]
	v_cmp_gt_i32_e64 s[10:11], 34, v171
	s_and_b64 s[12:13], s[14:15], s[12:13]
	v_cmp_gt_i32_e64 s[8:9], 33, v171
	s_and_b64 s[10:11], s[12:13], s[10:11]
	v_cmp_gt_i32_e32 vcc, 32, v171
	s_and_b64 s[8:9], s[10:11], s[8:9]
	v_cndmask_b32_e64 v85, v85, v147, s[44:45]
	s_mov_b32 s44, 0x41d00000
	v_cndmask_b32_e64 v84, v84, v147, s[42:43]
	s_mov_b32 s42, 0x41c00000
	v_cndmask_b32_e64 v83, v83, v147, s[40:41]
	s_mov_b32 s40, 0x41900000
	v_cndmask_b32_e64 v81, v81, v147, s[38:39]
	s_mov_b32 s38, 0x41800000
	v_cndmask_b32_e64 v80, v80, v147, s[36:37]
	s_mov_b32 s36, 0x41200000
	v_cndmask_b32_e64 v79, v79, v147, s[34:35]
	s_mov_b32 s34, 2.0
	s_and_b64 vcc, s[8:9], vcc
	v_cndmask_b32_e64 v97, v97, v147, s[68:69]
	v_cndmask_b32_e64 v96, v96, v147, s[66:67]
	v_cndmask_b32_e64 v95, v95, v147, s[64:65]
	v_cndmask_b32_e64 v94, v94, v147, s[62:63]
	v_cndmask_b32_e64 v93, v93, v147, s[60:61]
	v_cndmask_b32_e64 v92, v92, v147, s[58:59]
	v_cndmask_b32_e64 v91, v91, v147, s[56:57]
	v_cndmask_b32_e64 v90, v90, v147, s[54:55]
	v_cndmask_b32_e64 v89, v89, v147, s[52:53]
	v_cndmask_b32_e64 v88, v88, v147, s[50:51]
	v_cndmask_b32_e64 v87, v87, v147, s[48:49]
	v_cndmask_b32_e64 v86, v86, v147, s[46:47]
	s_mov_b32 s45, 0x41d80000
	s_mov_b32 s43, 0x41c80000
	s_mov_b32 s41, 0x41980000
	s_mov_b32 s39, 0x41880000
	s_mov_b32 s37, 0x41300000
	s_mov_b32 s35, 0x40400000
	v_cndmask_b32_e64 v78, v78, v147, s[30:31]
	v_cndmask_b32_e64 v77, v77, v147, s[28:29]
	v_cndmask_b32_e64 v76, v76, v147, s[26:27]
	v_cndmask_b32_e64 v75, v75, v147, s[24:25]
	v_cndmask_b32_e64 v74, v74, v147, s[22:23]
	v_cndmask_b32_e64 v73, v73, v147, s[20:21]
	v_cndmask_b32_e64 v72, v72, v147, s[18:19]
	v_cndmask_b32_e64 v71, v71, v147, s[16:17]
	v_cndmask_b32_e64 v70, v70, v147, s[14:15]
	v_cndmask_b32_e64 v69, v69, v147, s[12:13]
	v_cndmask_b32_e64 v68, v68, v147, s[10:11]
	v_cndmask_b32_e64 v67, v67, v147, s[8:9]
	v_cndmask_b32_e32 v66, v66, v147, vcc

; template <int DQK> __device__ __forceinline__ void partialSM(f32x16& p0, f32x16& p1, float& m_reg, float& mn, float& alpha) {
;     ...
;     const float mnL = -mn * C2;
; #pragma unroll
;     for (int r = 0; r < 16; ++r) p0[r] = fmaf(p0[r], C2, mnL);
; #pragma unroll
;     for (int r = 0; r < 16; ++r) p1[r] = fmaf(p1[r], C2, mnL);
; #pragma unroll
;     for (int r = 0; r < 16; ++r) p0[r] = __builtin_amdgcn_exp2f(p0[r]);
; }
; __device__ __forceinline__ void finishSM(f32x16& p0, f32x16& p1, float alpha, float& l_reg, bf16x8& pa0, bf16x8& pa1, bf16x8& pa2, bf16x8& pa3) {
; #pragma unroll
;     for (int r = 0; r < 16; ++r) p1[r] = __builtin_amdgcn_exp2f(p1[r]);
;     float ps = 0;
; #pragma unroll
;     for (int r = 0; r < 16; ++r) ps += p0[r];
; #pragma unroll
;     for (int r = 0; r < 16; ++r) ps += p1[r];
;     { auto rr = __builtin_amdgcn_permlane32_swap(__float_as_uint(ps), __float_as_uint(ps), false, false);
;       ps = __uint_as_float(rr[0]) + __uint_as_float(rr[1]); }
;     l_reg = l_reg * alpha + ps;
;     ...
;     PK4(p0, 0, pa0); PK4(p0, 8, pa1); PK4(p1, 0, pa2); PK4(p1, 8, pa3);
; template <int VB>
; __device__ __forceinline__ void pv_tile(f32x16* o, int vb0, bf16x8 pa0, bf16x8 pa1, bf16x8 pa2, bf16x8 pa3) {
;     ...
;     PV_D0(0); PV_D0(1); PV_D0(2); PV_D0(3);
.LBB0_698:
	v_cndmask_b32_e64 v137, v137, v173, s[8:9]
	v_mul_f32_e32 v173, 0xbe0293ee, v137
	v_fmamk_f32 v82, v82, 0x3e0293ee, v173
	v_fmamk_f32 v83, v83, 0x3e0293ee, v173
	v_fmamk_f32 v84, v84, 0x3e0293ee, v173
	v_fmamk_f32 v85, v85, 0x3e0293ee, v173
	v_fmamk_f32 v86, v86, 0x3e0293ee, v173
	v_fmamk_f32 v87, v87, 0x3e0293ee, v173
	v_fmamk_f32 v88, v88, 0x3e0293ee, v173
	v_fmamk_f32 v89, v89, 0x3e0293ee, v173
	v_fmamk_f32 v90, v90, 0x3e0293ee, v173
	v_fmamk_f32 v91, v91, 0x3e0293ee, v173
	v_fmamk_f32 v92, v92, 0x3e0293ee, v173
	v_fmamk_f32 v93, v93, 0x3e0293ee, v173
	v_fmamk_f32 v94, v94, 0x3e0293ee, v173
	v_fmamk_f32 v95, v95, 0x3e0293ee, v173
	v_fmamk_f32 v96, v96, 0x3e0293ee, v173
	v_fmamk_f32 v97, v97, 0x3e0293ee, v173
	v_fmamk_f32 v66, v66, 0x3e0293ee, v173
	v_fmamk_f32 v67, v67, 0x3e0293ee, v173
	v_fmamk_f32 v68, v68, 0x3e0293ee, v173
	v_fmamk_f32 v69, v69, 0x3e0293ee, v173
	v_fmamk_f32 v70, v70, 0x3e0293ee, v173
	v_fmamk_f32 v71, v71, 0x3e0293ee, v173
	v_fmamk_f32 v72, v72, 0x3e0293ee, v173
	v_fmamk_f32 v73, v73, 0x3e0293ee, v173
	v_fmamk_f32 v74, v74, 0x3e0293ee, v173
	v_fmamk_f32 v75, v75, 0x3e0293ee, v173
	v_fmamk_f32 v76, v76, 0x3e0293ee, v173
	v_fmamk_f32 v77, v77, 0x3e0293ee, v173
	v_fmamk_f32 v78, v78, 0x3e0293ee, v173
	v_fmamk_f32 v79, v79, 0x3e0293ee, v173
	v_fmamk_f32 v80, v80, 0x3e0293ee, v173
	v_fmac_f32_e32 v173, 0x3e0293ee, v81
	v_exp_f32_e32 v81, v82
	v_exp_f32_e32 v82, v83
	v_exp_f32_e32 v83, v84
	v_exp_f32_e32 v84, v85
	v_exp_f32_e32 v85, v86
	v_exp_f32_e32 v86, v87
	v_exp_f32_e32 v87, v88
	v_exp_f32_e32 v88, v89
	v_exp_f32_e32 v89, v90
	v_exp_f32_e32 v90, v91
	v_exp_f32_e32 v91, v92
	v_exp_f32_e32 v92, v93
	v_exp_f32_e32 v93, v94
	v_exp_f32_e32 v94, v95
	v_exp_f32_e32 v95, v96
	v_exp_f32_e32 v96, v97
	v_exp_f32_e32 v97, v66
	v_add_f32_e32 v66, 0, v81
	v_add_f32_e32 v66, v82, v66
	v_add_f32_e32 v66, v83, v66
	v_add_f32_e32 v66, v84, v66
	v_add_f32_e32 v66, v85, v66
	v_add_f32_e32 v66, v86, v66
	v_add_f32_e32 v66, v87, v66
	v_add_f32_e32 v66, v88, v66
	v_add_f32_e32 v66, v89, v66
	v_add_f32_e32 v66, v90, v66
	v_add_f32_e32 v66, v91, v66
	v_add_f32_e32 v66, v92, v66
	v_add_f32_e32 v66, v93, v66
	v_exp_f32_e32 v174, v67
	v_add_f32_e32 v66, v94, v66
	v_exp_f32_e32 v175, v68
	v_add_f32_e32 v66, v95, v66
	v_exp_f32_e32 v176, v69
	v_add_f32_e32 v66, v96, v66
	v_exp_f32_e32 v177, v70
	v_add_f32_e32 v66, v97, v66
	v_exp_f32_e32 v178, v71
	v_add_f32_e32 v66, v174, v66
	v_exp_f32_e32 v179, v72
	v_add_f32_e32 v66, v175, v66
	v_exp_f32_e32 v180, v73
	v_add_f32_e32 v66, v176, v66
	v_exp_f32_e32 v181, v74
	v_add_f32_e32 v66, v177, v66
	v_exp_f32_e32 v182, v75
	v_add_f32_e32 v66, v178, v66
	v_exp_f32_e32 v183, v76
	v_add_f32_e32 v66, v179, v66
	v_exp_f32_e32 v184, v77
	v_add_f32_e32 v66, v180, v66
	v_exp_f32_e32 v185, v78
	v_add_f32_e32 v66, v181, v66
	v_exp_f32_e32 v186, v79
	v_add_f32_e32 v66, v182, v66
	v_exp_f32_e32 v187, v80
	v_add_f32_e32 v66, v183, v66
	v_exp_f32_e32 v173, v173
	v_add_f32_e32 v66, v184, v66
	v_add_f32_e32 v66, v185, v66
	v_add_f32_e32 v66, v186, v66
	v_add_f32_e32 v66, v187, v66
	v_add_f32_e32 v66, v173, v66
	v_mov_b32_e32 v67, v66
	s_nop 1
	v_permlane32_swap_b32_e32 v66, v67
	v_add_f32_e32 v188, v66, v67
	v_cvt_pk_bf16_f32 v66, v81, v82
	v_cvt_pk_bf16_f32 v67, v83, v84
	v_cvt_pk_bf16_f32 v68, v85, v86
	v_cvt_pk_bf16_f32 v69, v87, v88
	v_cvt_pk_bf16_f32 v70, v89, v90
	v_cvt_pk_bf16_f32 v71, v91, v92
	v_cvt_pk_bf16_f32 v72, v93, v94
	v_cvt_pk_bf16_f32 v73, v95, v96
	v_cvt_pk_bf16_f32 v74, v97, v174
	v_cvt_pk_bf16_f32 v75, v175, v176
	v_cvt_pk_bf16_f32 v76, v177, v178
	v_cvt_pk_bf16_f32 v77, v179, v180
	v_cvt_pk_bf16_f32 v78, v181, v182
	v_cvt_pk_bf16_f32 v79, v183, v184
	v_cvt_pk_bf16_f32 v80, v185, v186
	v_cvt_pk_bf16_f32 v81, v187, v173
	v_fmac_f32_e32 v188, v145, v171
	v_permlane32_swap_b32_e32 v66, v68
	v_permlane32_swap_b32_e32 v67, v69
	v_permlane32_swap_b32_e32 v70, v72
	v_permlane32_swap_b32_e32 v71, v73
	v_permlane32_swap_b32_e32 v74, v76
	v_permlane32_swap_b32_e32 v75, v77
	v_permlane32_swap_b32_e32 v78, v80
	v_permlane32_swap_b32_e32 v79, v81
	ds_read_b64_tr_b16 v[82:83], v152 offset:0x4000
	ds_read_b64_tr_b16 v[84:85], v152 offset:0x4800
	ds_read_b64_tr_b16 v[86:87], v152 offset:0x5000
	ds_read_b64_tr_b16 v[88:89], v152 offset:0x5800
	ds_read_b64_tr_b16 v[90:91], v152 offset:0x6000
	ds_read_b64_tr_b16 v[92:93], v152 offset:0x6800
	ds_read_b64_tr_b16 v[94:95], v152 offset:0x7000
	ds_read_b64_tr_b16 v[96:97], v152 offset:0x7800
	s_waitcnt lgkmcnt(0)
	s_nop 0
	v_mfma_f32_32x32x16_bf16 v[18:33], v[66:69], v[82:85], v[18:33]
	ds_read_b64_tr_b16 v[82:83], v152 offset:0x4200
	ds_read_b64_tr_b16 v[84:85], v152 offset:0x4a00
	v_mfma_f32_32x32x16_bf16 v[18:33], v[70:73], v[86:89], v[18:33]
	ds_read_b64_tr_b16 v[86:87], v152 offset:0x5200
	ds_read_b64_tr_b16 v[88:89], v152 offset:0x5a00
	v_mfma_f32_32x32x16_bf16 v[18:33], v[74:77], v[90:93], v[18:33]
	ds_read_b64_tr_b16 v[90:91], v152 offset:0x6200
	ds_read_b64_tr_b16 v[92:93], v152 offset:0x6a00
	v_mfma_f32_32x32x16_bf16 v[18:33], v[78:81], v[94:97], v[18:33]
	ds_read_b64_tr_b16 v[94:95], v152 offset:0x7200
	ds_read_b64_tr_b16 v[96:97], v152 offset:0x7a00
	s_waitcnt lgkmcnt(0)
	v_mfma_f32_32x32x16_bf16 v[34:49], v[66:69], v[82:85], v[34:49]
	ds_read_b64_tr_b16 v[82:83], v152 offset:0x4400
	ds_read_b64_tr_b16 v[84:85], v152 offset:0x4c00
	v_mfma_f32_32x32x16_bf16 v[34:49], v[70:73], v[86:89], v[34:49]
	ds_read_b64_tr_b16 v[86:87], v152 offset:0x5400
	ds_read_b64_tr_b16 v[88:89], v152 offset:0x5c00
	v_mfma_f32_32x32x16_bf16 v[34:49], v[74:77], v[90:93], v[34:49]
	ds_read_b64_tr_b16 v[90:91], v152 offset:0x6400
	ds_read_b64_tr_b16 v[92:93], v152 offset:0x6c00
	v_mfma_f32_32x32x16_bf16 v[34:49], v[78:81], v[94:97], v[34:49]
	ds_read_b64_tr_b16 v[94:95], v152 offset:0x7400
	ds_read_b64_tr_b16 v[96:97], v152 offset:0x7c00
	s_waitcnt lgkmcnt(0)
	v_mfma_f32_32x32x16_bf16 v[50:65], v[66:69], v[82:85], v[50:65]
	ds_read_b64_tr_b16 v[82:83], v152 offset:0x4600
	ds_read_b64_tr_b16 v[84:85], v152 offset:0x4e00
	v_mfma_f32_32x32x16_bf16 v[50:65], v[70:73], v[86:89], v[50:65]
	ds_read_b64_tr_b16 v[86:87], v152 offset:0x5600
	ds_read_b64_tr_b16 v[88:89], v152 offset:0x5e00
	v_mfma_f32_32x32x16_bf16 v[50:65], v[74:77], v[90:93], v[50:65]
	ds_read_b64_tr_b16 v[90:91], v152 offset:0x6600
	ds_read_b64_tr_b16 v[92:93], v152 offset:0x6e00
	v_mfma_f32_32x32x16_bf16 v[50:65], v[78:81], v[94:97], v[50:65]
	ds_read_b64_tr_b16 v[94:95], v152 offset:0x7600
	ds_read_b64_tr_b16 v[96:97], v152 offset:0x7e00
	s_waitcnt lgkmcnt(0)
	v_mfma_f32_32x32x16_bf16 v[2:17], v[66:69], v[82:85], v[2:17]
	v_mov_b32_e32 v145, v188
	v_mfma_f32_32x32x16_bf16 v[2:17], v[70:73], v[86:89], v[2:17]
	v_mfma_f32_32x32x16_bf16 v[2:17], v[74:77], v[90:93], v[2:17]
	v_mfma_f32_32x32x16_bf16 v[2:17], v[78:81], v[94:97], v[2:17]
	s_cmp_lt_u32 s33, 3
	s_cbranch_scc1 .LBB0_561
; template <int DQK, int KB>
; __device__ __forceinline__ void qkt(f32x16& p0, f32x16& p1, const char* K_lds, int r32, int hi, const bf16x8* qr) {
;     constexpr int ROWB = DQK * 2, SHM_K = 64 * ROWB;
;     p0 = f32x16{}; p1 = f32x16{};
;     const char* kb[4];
; #pragma unroll
;     for (int dd = 0; dd < 4; ++dd) kb[dd] = K_lds + KB * SHM_K + r32 * ROWB + (((dd * 16 + hi * 8) * 2) ^ ((r32 & 7) << 4));
; #pragma unroll
;     for (int d0 = 0; d0 < DQK / 16; ++d0) { const char* a = kb[d0 & 3] + (d0 >> 2) * 128;
;         bf16x8 b0 = *reinterpret_cast<const bf16x8*>(a);
;         bf16x8 b1 = *reinterpret_cast<const bf16x8*>(a + 32 * ROWB);
;         p0 = __builtin_amdgcn_mfma_f32_32x32x16_bf16(b0, qr[d0], p0, 0, 0, 0);
;         p1 = __builtin_amdgcn_mfma_f32_32x32x16_bf16(b1, qr[d0], p1, 0, 0, 0); }
.LBB0_699:
	ds_read_b128 v[66:69], v166 offset:32768
	ds_read_b128 v[70:73], v166 offset:40960
	ds_read_b128 v[174:177], v167 offset:32768
	ds_read_b128 v[178:181], v167 offset:40960
	s_cmp_gt_u32 s80, 5
	s_waitcnt lgkmcnt(3)
	v_mfma_f32_32x32x16_bf16 v[82:97], v[66:69], v[126:129], 0
	s_waitcnt lgkmcnt(2)
	v_mfma_f32_32x32x16_bf16 v[66:81], v[70:73], v[126:129], 0
	s_waitcnt lgkmcnt(1)
	v_mfma_f32_32x32x16_bf16 v[82:97], v[174:177], v[122:125], v[82:97]
	s_waitcnt lgkmcnt(0)
	v_mfma_f32_32x32x16_bf16 v[66:81], v[178:181], v[122:125], v[66:81]
	ds_read_b128 v[174:177], v168 offset:32768
	ds_read_b128 v[178:181], v168 offset:40960
	s_waitcnt lgkmcnt(1)
	v_mfma_f32_32x32x16_bf16 v[82:97], v[174:177], v[118:121], v[82:97]
	s_waitcnt lgkmcnt(0)
	v_mfma_f32_32x32x16_bf16 v[66:81], v[178:181], v[118:121], v[66:81]
	ds_read_b128 v[174:177], v169 offset:32768
	ds_read_b128 v[178:181], v169 offset:40960
	s_waitcnt lgkmcnt(1)
	v_mfma_f32_32x32x16_bf16 v[82:97], v[174:177], v[114:117], v[82:97]
	s_waitcnt lgkmcnt(0)
	v_mfma_f32_32x32x16_bf16 v[66:81], v[178:181], v[114:117], v[66:81]
	ds_read_b128 v[174:177], v166 offset:32896
	ds_read_b128 v[178:181], v166 offset:41088
	s_waitcnt lgkmcnt(1)
	v_mfma_f32_32x32x16_bf16 v[82:97], v[174:177], v[110:113], v[82:97]
	s_waitcnt lgkmcnt(0)
	v_mfma_f32_32x32x16_bf16 v[66:81], v[178:181], v[110:113], v[66:81]
	ds_read_b128 v[174:177], v167 offset:32896
	ds_read_b128 v[178:181], v167 offset:41088
	s_waitcnt lgkmcnt(1)
	v_mfma_f32_32x32x16_bf16 v[82:97], v[174:177], v[106:109], v[82:97]
	s_waitcnt lgkmcnt(0)
	v_mfma_f32_32x32x16_bf16 v[66:81], v[178:181], v[106:109], v[66:81]
	ds_read_b128 v[174:177], v168 offset:32896
	ds_read_b128 v[178:181], v168 offset:41088
	s_waitcnt lgkmcnt(1)
	v_mfma_f32_32x32x16_bf16 v[82:97], v[174:177], v[102:105], v[82:97]
	s_waitcnt lgkmcnt(0)
	v_mfma_f32_32x32x16_bf16 v[66:81], v[178:181], v[102:105], v[66:81]
	ds_read_b128 v[174:177], v169 offset:32896
	ds_read_b128 v[178:181], v169 offset:41088
	s_waitcnt lgkmcnt(1)
	v_mfma_f32_32x32x16_bf16 v[82:97], v[174:177], v[98:101], v[82:97]
	v_mov_b32_e32 v174, v151
	s_nop 0
	v_mul_f32_e32 v176, v174, v158
	v_fma_f32 v182, v174, s34, v176
	v_fma_f32 v183, v174, s35, v176
	v_fma_f32 v184, v174, s2, v176
	v_fma_f32 v185, v174, s3, v176
	v_pk_fma_f32 v[186:187], v[174:175], s[36:37], v[176:177] op_sel_hi:[0,1,0]
	s_waitcnt lgkmcnt(0)
	v_mfma_f32_32x32x16_bf16 v[66:81], v[178:181], v[98:101], v[66:81]
	v_mov_b32_e32 v181, v174
	v_mul_f32_e32 v178, 0x42000000, v174
	v_fma_f32 v180, 0, v174, v176
	v_fmac_f32_e32 v181, v181, v158
	v_fma_f32 v188, v174, s38, v176
	v_fma_f32 v189, v174, s39, v176
	v_pk_fma_f32 v[190:191], v[174:175], s[40:41], v[176:177] op_sel_hi:[0,1,0]
	v_pk_fma_f32 v[192:193], v[174:175], s[42:43], v[176:177] op_sel_hi:[0,1,0]
	v_pk_fma_f32 v[174:175], v[174:175], s[44:45], v[176:177] op_sel_hi:[0,1,0]
	v_pk_add_f32 v[96:97], v[96:97], v[174:175]
	v_pk_add_f32 v[92:93], v[92:93], v[190:191]
	v_pk_add_f32 v[90:91], v[90:91], v[188:189]
	v_pk_add_f32 v[88:89], v[88:89], v[186:187]
	v_pk_add_f32 v[86:87], v[86:87], v[184:185]
	v_pk_add_f32 v[84:85], v[84:85], v[182:183]
	v_pk_add_f32 v[176:177], v[178:179], v[182:183] op_sel_hi:[0,1]
	v_pk_add_f32 v[182:183], v[178:179], v[184:185] op_sel_hi:[0,1]
	v_pk_add_f32 v[184:185], v[178:179], v[186:187] op_sel_hi:[0,1]
	v_pk_add_f32 v[186:187], v[178:179], v[188:189] op_sel_hi:[0,1]
	v_pk_add_f32 v[188:189], v[178:179], v[190:191] op_sel_hi:[0,1]
	v_pk_add_f32 v[190:191], v[178:179], v[192:193] op_sel_hi:[0,1]
	v_pk_add_f32 v[174:175], v[178:179], v[174:175] op_sel_hi:[0,1]
	v_pk_add_f32 v[178:179], v[178:179], v[180:181] op_sel_hi:[0,1]
	v_pk_add_f32 v[94:95], v[94:95], v[192:193]
	v_pk_add_f32 v[82:83], v[82:83], v[180:181]
	v_pk_add_f32 v[80:81], v[80:81], v[174:175]
	v_pk_add_f32 v[78:79], v[78:79], v[190:191]
	v_pk_add_f32 v[76:77], v[76:77], v[188:189]
	v_pk_add_f32 v[74:75], v[74:75], v[186:187]
	v_pk_add_f32 v[72:73], v[72:73], v[184:185]
	v_pk_add_f32 v[70:71], v[70:71], v[182:183]
	v_pk_add_f32 v[68:69], v[68:69], v[176:177]
	v_pk_add_f32 v[66:67], v[66:67], v[178:179]
	s_cbranch_scc1 .LBB0_701
; __device__ __forceinline__ void mask_tile(f32x16& p0, f32x16& p1, int dq) {
;     const float NEG = -__builtin_inff();
; #pragma unroll
;     for (int r = 0; r < 16; ++r) {
;         const int c = (r & 3) + 8 * (r >> 2);
;         if (dq - c < 0) p0[r] = NEG;
;         if (dq - c - 32 < 0) p1[r] = NEG;
;     }
; }
	v_sub_u32_e32 v171, v132, v154
	v_add_u32_e32 v171, 0xffffff80, v171
	v_cmp_gt_i32_e64 s[66:67], 26, v171
	v_cmp_gt_i32_e64 s[68:69], 27, v171
	v_cmp_gt_i32_e64 s[64:65], 25, v171
	s_and_b64 s[66:67], s[68:69], s[66:67]
	v_cmp_gt_i32_e64 s[62:63], 24, v171
	s_and_b64 s[64:65], s[66:67], s[64:65]
	v_cmp_gt_i32_e64 s[60:61], 19, v171
	s_and_b64 s[62:63], s[64:65], s[62:63]
	v_cmp_gt_i32_e64 s[58:59], 18, v171
	s_and_b64 s[60:61], s[62:63], s[60:61]
	v_cmp_gt_i32_e64 s[56:57], 17, v171
	s_and_b64 s[58:59], s[60:61], s[58:59]
	v_cmp_gt_i32_e64 s[54:55], 16, v171
	s_and_b64 s[56:57], s[58:59], s[56:57]
	v_cmp_gt_i32_e64 s[52:53], 11, v171
	s_and_b64 s[54:55], s[56:57], s[54:55]
	v_cmp_gt_i32_e64 s[50:51], 10, v171
	s_and_b64 s[52:53], s[54:55], s[52:53]
	v_cmp_gt_i32_e64 s[48:49], 9, v171
	s_and_b64 s[50:51], s[52:53], s[50:51]
	v_cmp_gt_i32_e64 s[46:47], 8, v171
	s_and_b64 s[48:49], s[50:51], s[48:49]
	v_cmp_gt_i32_e64 s[44:45], 3, v171
	s_and_b64 s[46:47], s[48:49], s[46:47]
	v_cmp_gt_i32_e64 s[42:43], 2, v171
	s_and_b64 s[44:45], s[46:47], s[44:45]
	v_cmp_gt_i32_e64 s[40:41], 1, v171
	s_and_b64 s[42:43], s[44:45], s[42:43]
	v_cmp_gt_i32_e64 s[38:39], 0, v171
	s_and_b64 s[40:41], s[42:43], s[40:41]
	s_and_b64 s[38:39], s[40:41], s[38:39]
	v_cmp_gt_i32_e64 s[36:37], 58, v171
	v_cndmask_b32_e64 v82, v82, v147, s[38:39]
	v_cmp_gt_i32_e64 s[38:39], 59, v171
	v_cmp_gt_i32_e64 s[34:35], 57, v171
	s_and_b64 s[36:37], s[38:39], s[36:37]
	v_cmp_gt_i32_e64 s[30:31], 56, v171
	s_and_b64 s[34:35], s[36:37], s[34:35]
	v_cmp_gt_i32_e64 s[28:29], 51, v171
	s_and_b64 s[30:31], s[34:35], s[30:31]
	v_cmp_gt_i32_e64 s[26:27], 50, v171
	s_and_b64 s[28:29], s[30:31], s[28:29]
	v_cmp_gt_i32_e64 s[24:25], 49, v171
	s_and_b64 s[26:27], s[28:29], s[26:27]
	v_cmp_gt_i32_e64 s[22:23], 48, v171
	s_and_b64 s[24:25], s[26:27], s[24:25]
	v_cmp_gt_i32_e64 s[20:21], 43, v171
	s_and_b64 s[22:23], s[24:25], s[22:23]
	v_cmp_gt_i32_e64 s[18:19], 42, v171
	s_and_b64 s[20:21], s[22:23], s[20:21]
	v_cmp_gt_i32_e64 s[16:17], 41, v171
	s_and_b64 s[18:19], s[20:21], s[18:19]
	v_cmp_gt_i32_e64 s[14:15], 40, v171
	s_and_b64 s[16:17], s[18:19], s[16:17]
	v_cmp_gt_i32_e64 s[12:13], 35, v171
	s_and_b64 s[14:15], s[16:17], s[14:15]
	v_cmp_gt_i32_e64 s[10:11], 34, v171
	s_and_b64 s[12:13], s[14:15], s[12:13]
	v_cmp_gt_i32_e64 s[8:9], 33, v171
	s_and_b64 s[10:11], s[12:13], s[10:11]
	v_cmp_gt_i32_e32 vcc, 32, v171
	s_and_b64 s[8:9], s[10:11], s[8:9]
	v_cndmask_b32_e64 v85, v85, v147, s[44:45]
	s_mov_b32 s44, 0x41d00000
	v_cndmask_b32_e64 v84, v84, v147, s[42:43]
	s_mov_b32 s42, 0x41c00000
	v_cndmask_b32_e64 v83, v83, v147, s[40:41]
	s_mov_b32 s40, 0x41900000
	v_cndmask_b32_e64 v81, v81, v147, s[38:39]
	s_mov_b32 s38, 0x41800000
	v_cndmask_b32_e64 v80, v80, v147, s[36:37]
	s_mov_b32 s36, 0x41200000
	v_cndmask_b32_e64 v79, v79, v147, s[34:35]
	s_mov_b32 s34, 2.0
	s_and_b64 vcc, s[8:9], vcc
	v_cndmask_b32_e64 v97, v97, v147, s[68:69]
	v_cndmask_b32_e64 v96, v96, v147, s[66:67]
	v_cndmask_b32_e64 v95, v95, v147, s[64:65]
	v_cndmask_b32_e64 v94, v94, v147, s[62:63]
	v_cndmask_b32_e64 v93, v93, v147, s[60:61]
	v_cndmask_b32_e64 v92, v92, v147, s[58:59]
	v_cndmask_b32_e64 v91, v91, v147, s[56:57]
	v_cndmask_b32_e64 v90, v90, v147, s[54:55]
	v_cndmask_b32_e64 v89, v89, v147, s[52:53]
	v_cndmask_b32_e64 v88, v88, v147, s[50:51]
	v_cndmask_b32_e64 v87, v87, v147, s[48:49]
	v_cndmask_b32_e64 v86, v86, v147, s[46:47]
	s_mov_b32 s45, 0x41d80000
	s_mov_b32 s43, 0x41c80000
	s_mov_b32 s41, 0x41980000
	s_mov_b32 s39, 0x41880000
	s_mov_b32 s37, 0x41300000
	s_mov_b32 s35, 0x40400000
	v_cndmask_b32_e64 v78, v78, v147, s[30:31]
	v_cndmask_b32_e64 v77, v77, v147, s[28:29]
	v_cndmask_b32_e64 v76, v76, v147, s[26:27]
	v_cndmask_b32_e64 v75, v75, v147, s[24:25]
	v_cndmask_b32_e64 v74, v74, v147, s[22:23]
	v_cndmask_b32_e64 v73, v73, v147, s[20:21]
	v_cndmask_b32_e64 v72, v72, v147, s[18:19]
	v_cndmask_b32_e64 v71, v71, v147, s[16:17]
	v_cndmask_b32_e64 v70, v70, v147, s[14:15]
	v_cndmask_b32_e64 v69, v69, v147, s[12:13]
	v_cndmask_b32_e64 v68, v68, v147, s[10:11]
	v_cndmask_b32_e64 v67, v67, v147, s[8:9]
	v_cndmask_b32_e32 v66, v66, v147, vcc

; template <int DQK> __device__ __forceinline__ void partialSM(f32x16& p0, f32x16& p1, float& m_reg, float& mn, float& alpha) {
;     ...
;     const float mnL = -mn * C2;
; #pragma unroll
;     for (int r = 0; r < 16; ++r) p0[r] = fmaf(p0[r], C2, mnL);
; #pragma unroll
;     for (int r = 0; r < 16; ++r) p1[r] = fmaf(p1[r], C2, mnL);
; #pragma unroll
;     for (int r = 0; r < 16; ++r) p0[r] = __builtin_amdgcn_exp2f(p0[r]);
; }
; __device__ __forceinline__ void finishSM(f32x16& p0, f32x16& p1, float alpha, float& l_reg, bf16x8& pa0, bf16x8& pa1, bf16x8& pa2, bf16x8& pa3) {
; #pragma unroll
;     for (int r = 0; r < 16; ++r) p1[r] = __builtin_amdgcn_exp2f(p1[r]);
;     float ps = 0;
; #pragma unroll
;     for (int r = 0; r < 16; ++r) ps += p0[r];
; #pragma unroll
;     for (int r = 0; r < 16; ++r) ps += p1[r];
;     { auto rr = __builtin_amdgcn_permlane32_swap(__float_as_uint(ps), __float_as_uint(ps), false, false);
;       ps = __uint_as_float(rr[0]) + __uint_as_float(rr[1]); }
;     l_reg = l_reg * alpha + ps;
;     ...
;     PK4(p0, 0, pa0); PK4(p0, 8, pa1); PK4(p1, 0, pa2); PK4(p1, 8, pa3);
; template <int VB>
; __device__ __forceinline__ void pv_tile(f32x16* o, int vb0, bf16x8 pa0, bf16x8 pa1, bf16x8 pa2, bf16x8 pa3) {
;     ...
;     PV_D0(0); PV_D0(1); PV_D0(2); PV_D0(3);
.LBB0_705:
	v_cndmask_b32_e64 v137, v137, v173, s[8:9]
	v_mul_f32_e32 v173, 0xbe0293ee, v137
	v_fmamk_f32 v82, v82, 0x3e0293ee, v173
	v_fmamk_f32 v83, v83, 0x3e0293ee, v173
	v_fmamk_f32 v84, v84, 0x3e0293ee, v173
	v_fmamk_f32 v85, v85, 0x3e0293ee, v173
	v_fmamk_f32 v86, v86, 0x3e0293ee, v173
	v_fmamk_f32 v87, v87, 0x3e0293ee, v173
	v_fmamk_f32 v88, v88, 0x3e0293ee, v173
	v_fmamk_f32 v89, v89, 0x3e0293ee, v173
	v_fmamk_f32 v90, v90, 0x3e0293ee, v173
	v_fmamk_f32 v91, v91, 0x3e0293ee, v173
	v_fmamk_f32 v92, v92, 0x3e0293ee, v173
	v_fmamk_f32 v93, v93, 0x3e0293ee, v173
	v_fmamk_f32 v94, v94, 0x3e0293ee, v173
	v_fmamk_f32 v95, v95, 0x3e0293ee, v173
	v_fmamk_f32 v96, v96, 0x3e0293ee, v173
	v_fmamk_f32 v97, v97, 0x3e0293ee, v173
	v_fmamk_f32 v66, v66, 0x3e0293ee, v173
	v_fmamk_f32 v67, v67, 0x3e0293ee, v173
	v_fmamk_f32 v68, v68, 0x3e0293ee, v173
	v_fmamk_f32 v69, v69, 0x3e0293ee, v173
	v_fmamk_f32 v70, v70, 0x3e0293ee, v173
	v_fmamk_f32 v71, v71, 0x3e0293ee, v173
	v_fmamk_f32 v72, v72, 0x3e0293ee, v173
	v_fmamk_f32 v73, v73, 0x3e0293ee, v173
	v_fmamk_f32 v74, v74, 0x3e0293ee, v173
	v_fmamk_f32 v75, v75, 0x3e0293ee, v173
	v_fmamk_f32 v76, v76, 0x3e0293ee, v173
	v_fmamk_f32 v77, v77, 0x3e0293ee, v173
	v_fmamk_f32 v78, v78, 0x3e0293ee, v173
	v_fmamk_f32 v79, v79, 0x3e0293ee, v173
	v_fmamk_f32 v80, v80, 0x3e0293ee, v173
	v_fmac_f32_e32 v173, 0x3e0293ee, v81
	v_exp_f32_e32 v81, v82
	v_exp_f32_e32 v82, v83
	v_exp_f32_e32 v83, v84
	v_exp_f32_e32 v84, v85
	v_exp_f32_e32 v85, v86
	v_exp_f32_e32 v86, v87
	v_exp_f32_e32 v87, v88
	v_exp_f32_e32 v88, v89
	v_exp_f32_e32 v89, v90
	v_exp_f32_e32 v90, v91
	v_exp_f32_e32 v91, v92
	v_exp_f32_e32 v92, v93
	v_exp_f32_e32 v93, v94
	v_exp_f32_e32 v94, v95
	v_exp_f32_e32 v95, v96
	v_exp_f32_e32 v96, v97
	v_exp_f32_e32 v97, v66
	v_add_f32_e32 v66, 0, v81
	v_add_f32_e32 v66, v82, v66
	v_add_f32_e32 v66, v83, v66
	v_add_f32_e32 v66, v84, v66
	v_add_f32_e32 v66, v85, v66
	v_add_f32_e32 v66, v86, v66
	v_add_f32_e32 v66, v87, v66
	v_add_f32_e32 v66, v88, v66
	v_add_f32_e32 v66, v89, v66
	v_add_f32_e32 v66, v90, v66
	v_add_f32_e32 v66, v91, v66
	v_add_f32_e32 v66, v92, v66
	v_add_f32_e32 v66, v93, v66
	v_exp_f32_e32 v174, v67
	v_add_f32_e32 v66, v94, v66
	v_exp_f32_e32 v175, v68
	v_add_f32_e32 v66, v95, v66
	v_exp_f32_e32 v176, v69
	v_add_f32_e32 v66, v96, v66
	v_exp_f32_e32 v177, v70
	v_add_f32_e32 v66, v97, v66
	v_exp_f32_e32 v178, v71
	v_add_f32_e32 v66, v174, v66
	v_exp_f32_e32 v179, v72
	v_add_f32_e32 v66, v175, v66
	v_exp_f32_e32 v180, v73
	v_add_f32_e32 v66, v176, v66
	v_exp_f32_e32 v181, v74
	v_add_f32_e32 v66, v177, v66
	v_exp_f32_e32 v182, v75
	v_add_f32_e32 v66, v178, v66
	v_exp_f32_e32 v183, v76
	v_add_f32_e32 v66, v179, v66
	v_exp_f32_e32 v184, v77
	v_add_f32_e32 v66, v180, v66
	v_exp_f32_e32 v185, v78
	v_add_f32_e32 v66, v181, v66
	v_exp_f32_e32 v186, v79
	v_add_f32_e32 v66, v182, v66
	v_exp_f32_e32 v187, v80
	v_add_f32_e32 v66, v183, v66
	v_exp_f32_e32 v173, v173
	v_add_f32_e32 v66, v184, v66
	v_add_f32_e32 v66, v185, v66
	v_add_f32_e32 v66, v186, v66
	v_add_f32_e32 v66, v187, v66
	v_add_f32_e32 v66, v173, v66
	v_mov_b32_e32 v67, v66
	s_nop 1
	v_permlane32_swap_b32_e32 v66, v67
	v_add_f32_e32 v188, v66, v67
	v_cvt_pk_bf16_f32 v66, v81, v82
	v_cvt_pk_bf16_f32 v67, v83, v84
	v_cvt_pk_bf16_f32 v68, v85, v86
	v_cvt_pk_bf16_f32 v69, v87, v88
	v_cvt_pk_bf16_f32 v70, v89, v90
	v_cvt_pk_bf16_f32 v71, v91, v92
	v_cvt_pk_bf16_f32 v72, v93, v94
	v_cvt_pk_bf16_f32 v73, v95, v96
	v_cvt_pk_bf16_f32 v74, v97, v174
	v_cvt_pk_bf16_f32 v75, v175, v176
	v_cvt_pk_bf16_f32 v76, v177, v178
	v_cvt_pk_bf16_f32 v77, v179, v180
	v_cvt_pk_bf16_f32 v78, v181, v182
	v_cvt_pk_bf16_f32 v79, v183, v184
	v_cvt_pk_bf16_f32 v80, v185, v186
	v_cvt_pk_bf16_f32 v81, v187, v173
	v_fmac_f32_e32 v188, v145, v171
	v_permlane32_swap_b32_e32 v66, v68
	v_permlane32_swap_b32_e32 v67, v69
	v_permlane32_swap_b32_e32 v70, v72
	v_permlane32_swap_b32_e32 v71, v73
	v_permlane32_swap_b32_e32 v74, v76
	v_permlane32_swap_b32_e32 v75, v77
	v_permlane32_swap_b32_e32 v78, v80
	v_permlane32_swap_b32_e32 v79, v81
	ds_read_b64_tr_b16 v[82:83], v152 offset:0x8000
	ds_read_b64_tr_b16 v[84:85], v152 offset:0x8800
	ds_read_b64_tr_b16 v[86:87], v152 offset:0x9000
	ds_read_b64_tr_b16 v[88:89], v152 offset:0x9800
	ds_read_b64_tr_b16 v[90:91], v152 offset:0xa000
	ds_read_b64_tr_b16 v[92:93], v152 offset:0xa800
	ds_read_b64_tr_b16 v[94:95], v152 offset:0xb000
	ds_read_b64_tr_b16 v[96:97], v152 offset:0xb800
	s_waitcnt lgkmcnt(0)
	s_nop 0
	v_mfma_f32_32x32x16_bf16 v[18:33], v[66:69], v[82:85], v[18:33]
	ds_read_b64_tr_b16 v[82:83], v152 offset:0x8200
	ds_read_b64_tr_b16 v[84:85], v152 offset:0x8a00
	v_mfma_f32_32x32x16_bf16 v[18:33], v[70:73], v[86:89], v[18:33]
	ds_read_b64_tr_b16 v[86:87], v152 offset:0x9200
	ds_read_b64_tr_b16 v[88:89], v152 offset:0x9a00
	v_mfma_f32_32x32x16_bf16 v[18:33], v[74:77], v[90:93], v[18:33]
	ds_read_b64_tr_b16 v[90:91], v152 offset:0xa200
	ds_read_b64_tr_b16 v[92:93], v152 offset:0xaa00
	v_mfma_f32_32x32x16_bf16 v[18:33], v[78:81], v[94:97], v[18:33]
	ds_read_b64_tr_b16 v[94:95], v152 offset:0xb200
	ds_read_b64_tr_b16 v[96:97], v152 offset:0xba00
	s_waitcnt lgkmcnt(0)
	v_mfma_f32_32x32x16_bf16 v[34:49], v[66:69], v[82:85], v[34:49]
	ds_read_b64_tr_b16 v[82:83], v152 offset:0x8400
	ds_read_b64_tr_b16 v[84:85], v152 offset:0x8c00
	v_mfma_f32_32x32x16_bf16 v[34:49], v[70:73], v[86:89], v[34:49]
	ds_read_b64_tr_b16 v[86:87], v152 offset:0x9400
	ds_read_b64_tr_b16 v[88:89], v152 offset:0x9c00
	v_mfma_f32_32x32x16_bf16 v[34:49], v[74:77], v[90:93], v[34:49]
	ds_read_b64_tr_b16 v[90:91], v152 offset:0xa400
	ds_read_b64_tr_b16 v[92:93], v152 offset:0xac00
	v_mfma_f32_32x32x16_bf16 v[34:49], v[78:81], v[94:97], v[34:49]
	ds_read_b64_tr_b16 v[94:95], v152 offset:0xb400
	ds_read_b64_tr_b16 v[96:97], v152 offset:0xbc00
	s_waitcnt lgkmcnt(0)
	v_mfma_f32_32x32x16_bf16 v[50:65], v[66:69], v[82:85], v[50:65]
	ds_read_b64_tr_b16 v[82:83], v152 offset:0x8600
	ds_read_b64_tr_b16 v[84:85], v152 offset:0x8e00
	v_mfma_f32_32x32x16_bf16 v[50:65], v[70:73], v[86:89], v[50:65]
	ds_read_b64_tr_b16 v[86:87], v152 offset:0x9600
	ds_read_b64_tr_b16 v[88:89], v152 offset:0x9e00
	v_mfma_f32_32x32x16_bf16 v[50:65], v[74:77], v[90:93], v[50:65]
	ds_read_b64_tr_b16 v[90:91], v152 offset:0xa600
	ds_read_b64_tr_b16 v[92:93], v152 offset:0xae00
	v_mfma_f32_32x32x16_bf16 v[50:65], v[78:81], v[94:97], v[50:65]
	ds_read_b64_tr_b16 v[94:95], v152 offset:0xb600
	ds_read_b64_tr_b16 v[96:97], v152 offset:0xbe00
	s_waitcnt lgkmcnt(0)
	v_mfma_f32_32x32x16_bf16 v[2:17], v[66:69], v[82:85], v[2:17]
	v_mov_b32_e32 v145, v188
	v_mfma_f32_32x32x16_bf16 v[2:17], v[70:73], v[86:89], v[2:17]
	v_mfma_f32_32x32x16_bf16 v[2:17], v[74:77], v[90:93], v[2:17]
	v_mfma_f32_32x32x16_bf16 v[2:17], v[78:81], v[94:97], v[2:17]
	s_cmp_lt_u32 s33, 4
	s_cbranch_scc1 .LBB0_562
; template <int DQK, int KB>
; __device__ __forceinline__ void qkt(f32x16& p0, f32x16& p1, const char* K_lds, int r32, int hi, const bf16x8* qr) {
;     constexpr int ROWB = DQK * 2, SHM_K = 64 * ROWB;
;     p0 = f32x16{}; p1 = f32x16{};
;     const char* kb[4];
; #pragma unroll
;     for (int dd = 0; dd < 4; ++dd) kb[dd] = K_lds + KB * SHM_K + r32 * ROWB + (((dd * 16 + hi * 8) * 2) ^ ((r32 & 7) << 4));
; #pragma unroll
;     for (int d0 = 0; d0 < DQK / 16; ++d0) { const char* a = kb[d0 & 3] + (d0 >> 2) * 128;
;         bf16x8 b0 = *reinterpret_cast<const bf16x8*>(a);
;         bf16x8 b1 = *reinterpret_cast<const bf16x8*>(a + 32 * ROWB);
;         p0 = __builtin_amdgcn_mfma_f32_32x32x16_bf16(b0, qr[d0], p0, 0, 0, 0);
;         p1 = __builtin_amdgcn_mfma_f32_32x32x16_bf16(b1, qr[d0], p1, 0, 0, 0); }
.LBB0_706:
	ds_read_b128 v[66:69], v166 offset:49152
	ds_read_b128 v[70:73], v166 offset:57344
	s_andn2_b64 vcc, exec, s[74:75]
	s_waitcnt lgkmcnt(1)
	v_mfma_f32_32x32x16_bf16 v[82:97], v[66:69], v[126:129], 0
	s_waitcnt lgkmcnt(0)
	v_mfma_f32_32x32x16_bf16 v[66:81], v[70:73], v[126:129], 0
	ds_read_b128 v[126:129], v167 offset:49152
	ds_read_b128 v[174:177], v167 offset:57344
	s_waitcnt lgkmcnt(1)
	v_mfma_f32_32x32x16_bf16 v[82:97], v[126:129], v[122:125], v[82:97]
	s_waitcnt lgkmcnt(0)
	v_mfma_f32_32x32x16_bf16 v[66:81], v[174:177], v[122:125], v[66:81]
	ds_read_b128 v[122:125], v168 offset:49152
	ds_read_b128 v[126:129], v168 offset:57344
	s_waitcnt lgkmcnt(1)
	v_mfma_f32_32x32x16_bf16 v[82:97], v[122:125], v[118:121], v[82:97]
	s_waitcnt lgkmcnt(0)
	v_mfma_f32_32x32x16_bf16 v[66:81], v[126:129], v[118:121], v[66:81]
	ds_read_b128 v[118:121], v169 offset:49152
	ds_read_b128 v[122:125], v169 offset:57344
	s_waitcnt lgkmcnt(1)
	v_mfma_f32_32x32x16_bf16 v[82:97], v[118:121], v[114:117], v[82:97]
	s_waitcnt lgkmcnt(0)
	v_mfma_f32_32x32x16_bf16 v[66:81], v[122:125], v[114:117], v[66:81]
	ds_read_b128 v[114:117], v166 offset:49280
	ds_read_b128 v[118:121], v166 offset:57472
	s_waitcnt lgkmcnt(1)
	v_mfma_f32_32x32x16_bf16 v[82:97], v[114:117], v[110:113], v[82:97]
	s_waitcnt lgkmcnt(0)
	v_mfma_f32_32x32x16_bf16 v[66:81], v[118:121], v[110:113], v[66:81]
	ds_read_b128 v[110:113], v167 offset:49280
	ds_read_b128 v[114:117], v167 offset:57472
	s_waitcnt lgkmcnt(1)
	v_mfma_f32_32x32x16_bf16 v[82:97], v[110:113], v[106:109], v[82:97]
	s_waitcnt lgkmcnt(0)
	v_mfma_f32_32x32x16_bf16 v[66:81], v[114:117], v[106:109], v[66:81]
	ds_read_b128 v[106:109], v168 offset:49280
	ds_read_b128 v[110:113], v168 offset:57472
	s_waitcnt lgkmcnt(1)
	v_mfma_f32_32x32x16_bf16 v[82:97], v[106:109], v[102:105], v[82:97]
	s_waitcnt lgkmcnt(0)
	v_mfma_f32_32x32x16_bf16 v[66:81], v[110:113], v[102:105], v[66:81]
	ds_read_b128 v[102:105], v169 offset:49280
	ds_read_b128 v[106:109], v169 offset:57472
	s_waitcnt lgkmcnt(1)
	v_mfma_f32_32x32x16_bf16 v[82:97], v[102:105], v[98:101], v[82:97]
	s_waitcnt lgkmcnt(0)
	v_mfma_f32_32x32x16_bf16 v[66:81], v[106:109], v[98:101], v[66:81]
	v_mov_b32_e32 v98, v151
	s_nop 0
	v_mul_f32_e32 v100, v98, v159
	v_mov_b32_e32 v105, v98
	v_mul_f32_e32 v102, 0x42000000, v98
	v_fma_f32 v104, 0, v98, v100
	v_fmac_f32_e32 v105, v105, v159
	v_pk_fma_f32 v[106:107], v[98:99], s[34:35], v[100:101] op_sel_hi:[0,1,0]
	v_pk_fma_f32 v[108:109], v[98:99], s[2:3], v[100:101] op_sel_hi:[0,1,0]
	v_pk_fma_f32 v[110:111], v[98:99], s[36:37], v[100:101] op_sel_hi:[0,1,0]
	v_pk_fma_f32 v[112:113], v[98:99], s[38:39], v[100:101] op_sel_hi:[0,1,0]
	v_pk_fma_f32 v[114:115], v[98:99], s[40:41], v[100:101] op_sel_hi:[0,1,0]
	v_pk_fma_f32 v[116:117], v[98:99], s[42:43], v[100:101] op_sel_hi:[0,1,0]
	v_pk_fma_f32 v[98:99], v[98:99], s[44:45], v[100:101] op_sel_hi:[0,1,0]
	v_pk_add_f32 v[96:97], v[96:97], v[98:99]
	v_pk_add_f32 v[92:93], v[92:93], v[114:115]
	v_pk_add_f32 v[90:91], v[90:91], v[112:113]
	v_pk_add_f32 v[88:89], v[88:89], v[110:111]
	v_pk_add_f32 v[86:87], v[86:87], v[108:109]
	v_pk_add_f32 v[84:85], v[84:85], v[106:107]
	v_pk_add_f32 v[100:101], v[102:103], v[106:107] op_sel_hi:[0,1]
	v_pk_add_f32 v[106:107], v[102:103], v[108:109] op_sel_hi:[0,1]
	v_pk_add_f32 v[108:109], v[102:103], v[110:111] op_sel_hi:[0,1]
	v_pk_add_f32 v[110:111], v[102:103], v[112:113] op_sel_hi:[0,1]
	v_pk_add_f32 v[112:113], v[102:103], v[114:115] op_sel_hi:[0,1]
	v_pk_add_f32 v[114:115], v[102:103], v[116:117] op_sel_hi:[0,1]
	v_pk_add_f32 v[98:99], v[102:103], v[98:99] op_sel_hi:[0,1]
	v_pk_add_f32 v[102:103], v[102:103], v[104:105] op_sel_hi:[0,1]
	v_pk_add_f32 v[94:95], v[94:95], v[116:117]
	v_pk_add_f32 v[82:83], v[82:83], v[104:105]
	v_pk_add_f32 v[80:81], v[80:81], v[98:99]
	v_pk_add_f32 v[78:79], v[78:79], v[114:115]
	v_pk_add_f32 v[76:77], v[76:77], v[112:113]
	v_pk_add_f32 v[74:75], v[74:75], v[110:111]
	v_pk_add_f32 v[72:73], v[72:73], v[108:109]
	v_pk_add_f32 v[70:71], v[70:71], v[106:107]
	v_pk_add_f32 v[68:69], v[68:69], v[100:101]
	v_pk_add_f32 v[66:67], v[66:67], v[102:103]
	s_cbranch_vccnz .LBB0_708
; __device__ __forceinline__ void mask_tile(f32x16& p0, f32x16& p1, int dq) {
;     const float NEG = -__builtin_inff();
; #pragma unroll
;     for (int r = 0; r < 16; ++r) {
;         const int c = (r & 3) + 8 * (r >> 2);
;         if (dq - c < 0) p0[r] = NEG;
;         if (dq - c - 32 < 0) p1[r] = NEG;
;     }
; }
	v_sub_u32_e32 v98, v132, v154
	v_add_u32_e32 v98, 0xffffff40, v98
	v_cmp_gt_i32_e64 s[66:67], 26, v98
	v_cmp_gt_i32_e64 s[68:69], 27, v98
	v_cmp_gt_i32_e64 s[64:65], 25, v98
	s_and_b64 s[66:67], s[68:69], s[66:67]
	v_cmp_gt_i32_e64 s[62:63], 24, v98
	s_and_b64 s[64:65], s[66:67], s[64:65]
	v_cmp_gt_i32_e64 s[60:61], 19, v98
	s_and_b64 s[62:63], s[64:65], s[62:63]
	v_cmp_gt_i32_e64 s[58:59], 18, v98
	s_and_b64 s[60:61], s[62:63], s[60:61]
	v_cmp_gt_i32_e64 s[56:57], 17, v98
	s_and_b64 s[58:59], s[60:61], s[58:59]
	v_cmp_gt_i32_e64 s[54:55], 16, v98
	s_and_b64 s[56:57], s[58:59], s[56:57]
	v_cmp_gt_i32_e64 s[52:53], 11, v98
	s_and_b64 s[54:55], s[56:57], s[54:55]
	v_cmp_gt_i32_e64 s[50:51], 10, v98
	s_and_b64 s[52:53], s[54:55], s[52:53]
	v_cmp_gt_i32_e64 s[48:49], 9, v98
	s_and_b64 s[50:51], s[52:53], s[50:51]
	v_cmp_gt_i32_e64 s[46:47], 8, v98
	s_and_b64 s[48:49], s[50:51], s[48:49]
	v_cmp_gt_i32_e64 s[44:45], 3, v98
	s_and_b64 s[46:47], s[48:49], s[46:47]
	v_cmp_gt_i32_e64 s[42:43], 2, v98
	s_and_b64 s[44:45], s[46:47], s[44:45]
	v_cmp_gt_i32_e64 s[40:41], 1, v98
	s_and_b64 s[42:43], s[44:45], s[42:43]
	v_cmp_gt_i32_e64 s[38:39], 0, v98
	s_and_b64 s[40:41], s[42:43], s[40:41]
	s_and_b64 s[38:39], s[40:41], s[38:39]
	v_cmp_gt_i32_e64 s[36:37], 58, v98
	v_cndmask_b32_e64 v82, v82, v147, s[38:39]
	v_cmp_gt_i32_e64 s[38:39], 59, v98
	v_cmp_gt_i32_e64 s[34:35], 57, v98
	s_and_b64 s[36:37], s[38:39], s[36:37]
	v_cmp_gt_i32_e64 s[30:31], 56, v98
	s_and_b64 s[34:35], s[36:37], s[34:35]
	v_cmp_gt_i32_e64 s[28:29], 51, v98
	s_and_b64 s[30:31], s[34:35], s[30:31]
	v_cmp_gt_i32_e64 s[26:27], 50, v98
	s_and_b64 s[28:29], s[30:31], s[28:29]
	v_cmp_gt_i32_e64 s[24:25], 49, v98
	s_and_b64 s[26:27], s[28:29], s[26:27]
	v_cmp_gt_i32_e64 s[22:23], 48, v98
	s_and_b64 s[24:25], s[26:27], s[24:25]
	v_cmp_gt_i32_e64 s[20:21], 43, v98
	s_and_b64 s[22:23], s[24:25], s[22:23]
	v_cmp_gt_i32_e64 s[18:19], 42, v98
	s_and_b64 s[20:21], s[22:23], s[20:21]
	v_cmp_gt_i32_e64 s[16:17], 41, v98
	s_and_b64 s[18:19], s[20:21], s[18:19]
	v_cmp_gt_i32_e64 s[14:15], 40, v98
	s_and_b64 s[16:17], s[18:19], s[16:17]
	v_cmp_gt_i32_e64 s[12:13], 35, v98
	s_and_b64 s[14:15], s[16:17], s[14:15]
	v_cmp_gt_i32_e64 s[10:11], 34, v98
	s_and_b64 s[12:13], s[14:15], s[12:13]
	v_cmp_gt_i32_e64 s[8:9], 33, v98
	s_and_b64 s[10:11], s[12:13], s[10:11]
	v_cmp_gt_i32_e32 vcc, 32, v98
	s_and_b64 s[8:9], s[10:11], s[8:9]
	v_cndmask_b32_e64 v85, v85, v147, s[44:45]
	s_mov_b32 s44, 0x41d00000
	v_cndmask_b32_e64 v84, v84, v147, s[42:43]
	s_mov_b32 s42, 0x41c00000
	v_cndmask_b32_e64 v83, v83, v147, s[40:41]
	s_mov_b32 s40, 0x41900000
	v_cndmask_b32_e64 v81, v81, v147, s[38:39]
	s_mov_b32 s38, 0x41800000
	v_cndmask_b32_e64 v80, v80, v147, s[36:37]
	s_mov_b32 s36, 0x41200000
	v_cndmask_b32_e64 v79, v79, v147, s[34:35]
	s_mov_b32 s34, 2.0
	s_and_b64 vcc, s[8:9], vcc
	v_cndmask_b32_e64 v97, v97, v147, s[68:69]
	v_cndmask_b32_e64 v96, v96, v147, s[66:67]
	v_cndmask_b32_e64 v95, v95, v147, s[64:65]
	v_cndmask_b32_e64 v94, v94, v147, s[62:63]
	v_cndmask_b32_e64 v93, v93, v147, s[60:61]
	v_cndmask_b32_e64 v92, v92, v147, s[58:59]
	v_cndmask_b32_e64 v91, v91, v147, s[56:57]
	v_cndmask_b32_e64 v90, v90, v147, s[54:55]
	v_cndmask_b32_e64 v89, v89, v147, s[52:53]
	v_cndmask_b32_e64 v88, v88, v147, s[50:51]
	v_cndmask_b32_e64 v87, v87, v147, s[48:49]
	v_cndmask_b32_e64 v86, v86, v147, s[46:47]
	s_mov_b32 s45, 0x41d80000
	s_mov_b32 s43, 0x41c80000
	s_mov_b32 s41, 0x41980000
	s_mov_b32 s39, 0x41880000
	s_mov_b32 s37, 0x41300000
	s_mov_b32 s35, 0x40400000
	v_cndmask_b32_e64 v78, v78, v147, s[30:31]
	v_cndmask_b32_e64 v77, v77, v147, s[28:29]
	v_cndmask_b32_e64 v76, v76, v147, s[26:27]
	v_cndmask_b32_e64 v75, v75, v147, s[24:25]
	v_cndmask_b32_e64 v74, v74, v147, s[22:23]
	v_cndmask_b32_e64 v73, v73, v147, s[20:21]
	v_cndmask_b32_e64 v72, v72, v147, s[18:19]
	v_cndmask_b32_e64 v71, v71, v147, s[16:17]
	v_cndmask_b32_e64 v70, v70, v147, s[14:15]
	v_cndmask_b32_e64 v69, v69, v147, s[12:13]
	v_cndmask_b32_e64 v68, v68, v147, s[10:11]
	v_cndmask_b32_e64 v67, v67, v147, s[8:9]
	v_cndmask_b32_e32 v66, v66, v147, vcc

; template <int DQK> __device__ __forceinline__ void partialSM(f32x16& p0, f32x16& p1, float& m_reg, float& mn, float& alpha) {
;     ...
;     const float mnL = -mn * C2;
; #pragma unroll
;     for (int r = 0; r < 16; ++r) p0[r] = fmaf(p0[r], C2, mnL);
; #pragma unroll
;     for (int r = 0; r < 16; ++r) p1[r] = fmaf(p1[r], C2, mnL);
; #pragma unroll
;     for (int r = 0; r < 16; ++r) p0[r] = __builtin_amdgcn_exp2f(p0[r]);
; }
; __device__ __forceinline__ void finishSM(f32x16& p0, f32x16& p1, float alpha, float& l_reg, bf16x8& pa0, bf16x8& pa1, bf16x8& pa2, bf16x8& pa3) {
; #pragma unroll
;     for (int r = 0; r < 16; ++r) p1[r] = __builtin_amdgcn_exp2f(p1[r]);
;     float ps = 0;
; #pragma unroll
;     for (int r = 0; r < 16; ++r) ps += p0[r];
; #pragma unroll
;     for (int r = 0; r < 16; ++r) ps += p1[r];
;     { auto rr = __builtin_amdgcn_permlane32_swap(__float_as_uint(ps), __float_as_uint(ps), false, false);
;       ps = __uint_as_float(rr[0]) + __uint_as_float(rr[1]); }
;     l_reg = l_reg * alpha + ps;
;     ...
;     PK4(p0, 0, pa0); PK4(p0, 8, pa1); PK4(p1, 0, pa2); PK4(p1, 8, pa3);
; template <int VB>
; __device__ __forceinline__ void pv_tile(f32x16* o, int vb0, bf16x8 pa0, bf16x8 pa1, bf16x8 pa2, bf16x8 pa3) {
;     ...
;     PV_D0(0); PV_D0(1); PV_D0(2); PV_D0(3);
.LBB0_712:
	v_cndmask_b32_e64 v137, v137, v99, s[8:9]
	v_mul_f32_e32 v99, 0xbe0293ee, v137
	v_fmamk_f32 v82, v82, 0x3e0293ee, v99
	v_fmamk_f32 v83, v83, 0x3e0293ee, v99
	v_fmamk_f32 v84, v84, 0x3e0293ee, v99
	v_fmamk_f32 v85, v85, 0x3e0293ee, v99
	v_fmamk_f32 v86, v86, 0x3e0293ee, v99
	v_fmamk_f32 v87, v87, 0x3e0293ee, v99
	v_fmamk_f32 v88, v88, 0x3e0293ee, v99
	v_fmamk_f32 v89, v89, 0x3e0293ee, v99
	v_fmamk_f32 v90, v90, 0x3e0293ee, v99
	v_fmamk_f32 v91, v91, 0x3e0293ee, v99
	v_fmamk_f32 v92, v92, 0x3e0293ee, v99
	v_fmamk_f32 v93, v93, 0x3e0293ee, v99
	v_fmamk_f32 v94, v94, 0x3e0293ee, v99
	v_fmamk_f32 v95, v95, 0x3e0293ee, v99
	v_fmamk_f32 v96, v96, 0x3e0293ee, v99
	v_fmamk_f32 v97, v97, 0x3e0293ee, v99
	v_fmamk_f32 v66, v66, 0x3e0293ee, v99
	v_fmamk_f32 v67, v67, 0x3e0293ee, v99
	v_fmamk_f32 v68, v68, 0x3e0293ee, v99
	v_fmamk_f32 v69, v69, 0x3e0293ee, v99
	v_fmamk_f32 v70, v70, 0x3e0293ee, v99
	v_fmamk_f32 v71, v71, 0x3e0293ee, v99
	v_fmamk_f32 v72, v72, 0x3e0293ee, v99
	v_fmamk_f32 v73, v73, 0x3e0293ee, v99
	v_fmamk_f32 v74, v74, 0x3e0293ee, v99
	v_fmamk_f32 v75, v75, 0x3e0293ee, v99
	v_fmamk_f32 v76, v76, 0x3e0293ee, v99
	v_fmamk_f32 v77, v77, 0x3e0293ee, v99
	v_fmamk_f32 v78, v78, 0x3e0293ee, v99
	v_fmamk_f32 v79, v79, 0x3e0293ee, v99
	v_fmamk_f32 v80, v80, 0x3e0293ee, v99
	v_fmac_f32_e32 v99, 0x3e0293ee, v81
	v_exp_f32_e32 v81, v82
	v_exp_f32_e32 v82, v83
	v_exp_f32_e32 v83, v84
	v_exp_f32_e32 v84, v85
	v_exp_f32_e32 v85, v86
	v_exp_f32_e32 v86, v87
	v_exp_f32_e32 v87, v88
	v_exp_f32_e32 v88, v89
	v_exp_f32_e32 v89, v90
	v_exp_f32_e32 v90, v91
	v_exp_f32_e32 v91, v92
	v_exp_f32_e32 v92, v93
	v_exp_f32_e32 v93, v94
	v_exp_f32_e32 v94, v95
	v_exp_f32_e32 v95, v96
	v_exp_f32_e32 v96, v97
	v_exp_f32_e32 v97, v66
	v_add_f32_e32 v66, 0, v81
	v_add_f32_e32 v66, v82, v66
	v_add_f32_e32 v66, v83, v66
	v_add_f32_e32 v66, v84, v66
	v_add_f32_e32 v66, v85, v66
	v_add_f32_e32 v66, v86, v66
	v_add_f32_e32 v66, v87, v66
	v_add_f32_e32 v66, v88, v66
	v_add_f32_e32 v66, v89, v66
	v_add_f32_e32 v66, v90, v66
	v_add_f32_e32 v66, v91, v66
	v_add_f32_e32 v66, v92, v66
	v_add_f32_e32 v66, v93, v66
	v_exp_f32_e32 v100, v67
	v_add_f32_e32 v66, v94, v66
	v_exp_f32_e32 v101, v68
	v_add_f32_e32 v66, v95, v66
	v_exp_f32_e32 v102, v69
	v_add_f32_e32 v66, v96, v66
	v_exp_f32_e32 v103, v70
	v_add_f32_e32 v66, v97, v66
	v_exp_f32_e32 v104, v71
	v_add_f32_e32 v66, v100, v66
	v_exp_f32_e32 v105, v72
	v_add_f32_e32 v66, v101, v66
	v_exp_f32_e32 v106, v73
	v_add_f32_e32 v66, v102, v66
	v_exp_f32_e32 v107, v74
	v_add_f32_e32 v66, v103, v66
	v_exp_f32_e32 v108, v75
	v_add_f32_e32 v66, v104, v66
	v_exp_f32_e32 v109, v76
	v_add_f32_e32 v66, v105, v66
	v_exp_f32_e32 v110, v77
	v_add_f32_e32 v66, v106, v66
	v_exp_f32_e32 v111, v78
	v_add_f32_e32 v66, v107, v66
	v_exp_f32_e32 v112, v79
	v_add_f32_e32 v66, v108, v66
	v_exp_f32_e32 v113, v80
	v_add_f32_e32 v66, v109, v66
	v_exp_f32_e32 v99, v99
	v_add_f32_e32 v66, v110, v66
	v_add_f32_e32 v66, v111, v66
	v_add_f32_e32 v66, v112, v66
	v_add_f32_e32 v66, v113, v66
	v_add_f32_e32 v66, v99, v66
	v_mov_b32_e32 v67, v66
	s_nop 1
	v_permlane32_swap_b32_e32 v66, v67
	v_add_f32_e32 v114, v66, v67
	v_cvt_pk_bf16_f32 v66, v81, v82
	v_cvt_pk_bf16_f32 v67, v83, v84
	v_cvt_pk_bf16_f32 v68, v85, v86
	v_cvt_pk_bf16_f32 v69, v87, v88
	v_cvt_pk_bf16_f32 v70, v89, v90
	v_cvt_pk_bf16_f32 v71, v91, v92
	v_cvt_pk_bf16_f32 v72, v93, v94
	v_cvt_pk_bf16_f32 v73, v95, v96
	v_cvt_pk_bf16_f32 v74, v97, v100
	v_cvt_pk_bf16_f32 v75, v101, v102
	v_cvt_pk_bf16_f32 v76, v103, v104
	v_cvt_pk_bf16_f32 v77, v105, v106
	v_cvt_pk_bf16_f32 v78, v107, v108
	v_cvt_pk_bf16_f32 v79, v109, v110
	v_cvt_pk_bf16_f32 v80, v111, v112
	v_cvt_pk_bf16_f32 v81, v113, v99
	v_fmac_f32_e32 v114, v145, v98
	v_permlane32_swap_b32_e32 v66, v68
	v_permlane32_swap_b32_e32 v67, v69
	v_permlane32_swap_b32_e32 v70, v72
	v_permlane32_swap_b32_e32 v71, v73
	v_permlane32_swap_b32_e32 v74, v76
	v_permlane32_swap_b32_e32 v75, v77
	v_permlane32_swap_b32_e32 v78, v80
	v_permlane32_swap_b32_e32 v79, v81
	ds_read_b64_tr_b16 v[82:83], v152 offset:0xc000
	ds_read_b64_tr_b16 v[84:85], v152 offset:0xc800
	ds_read_b64_tr_b16 v[86:87], v152 offset:0xd000
	ds_read_b64_tr_b16 v[88:89], v152 offset:0xd800
	ds_read_b64_tr_b16 v[90:91], v152 offset:0xe000
	ds_read_b64_tr_b16 v[92:93], v152 offset:0xe800
	ds_read_b64_tr_b16 v[94:95], v152 offset:0xf000
	ds_read_b64_tr_b16 v[96:97], v152 offset:0xf800
	s_waitcnt lgkmcnt(0)
	s_nop 0
	v_mfma_f32_32x32x16_bf16 v[18:33], v[66:69], v[82:85], v[18:33]
	ds_read_b64_tr_b16 v[82:83], v152 offset:0xc200
	ds_read_b64_tr_b16 v[84:85], v152 offset:0xca00
	v_mfma_f32_32x32x16_bf16 v[18:33], v[70:73], v[86:89], v[18:33]
	ds_read_b64_tr_b16 v[86:87], v152 offset:0xd200
	ds_read_b64_tr_b16 v[88:89], v152 offset:0xda00
	v_mfma_f32_32x32x16_bf16 v[18:33], v[74:77], v[90:93], v[18:33]
	ds_read_b64_tr_b16 v[90:91], v152 offset:0xe200
	ds_read_b64_tr_b16 v[92:93], v152 offset:0xea00
	v_mfma_f32_32x32x16_bf16 v[18:33], v[78:81], v[94:97], v[18:33]
	ds_read_b64_tr_b16 v[94:95], v152 offset:0xf200
	ds_read_b64_tr_b16 v[96:97], v152 offset:0xfa00
	s_waitcnt lgkmcnt(0)
	v_mfma_f32_32x32x16_bf16 v[34:49], v[66:69], v[82:85], v[34:49]
	ds_read_b64_tr_b16 v[82:83], v152 offset:0xc400
	ds_read_b64_tr_b16 v[84:85], v152 offset:0xcc00
	v_mfma_f32_32x32x16_bf16 v[34:49], v[70:73], v[86:89], v[34:49]
	ds_read_b64_tr_b16 v[86:87], v152 offset:0xd400
	ds_read_b64_tr_b16 v[88:89], v152 offset:0xdc00
	v_mfma_f32_32x32x16_bf16 v[34:49], v[74:77], v[90:93], v[34:49]
	ds_read_b64_tr_b16 v[90:91], v152 offset:0xe400
	ds_read_b64_tr_b16 v[92:93], v152 offset:0xec00
	v_mfma_f32_32x32x16_bf16 v[34:49], v[78:81], v[94:97], v[34:49]
	ds_read_b64_tr_b16 v[94:95], v152 offset:0xf400
	ds_read_b64_tr_b16 v[96:97], v152 offset:0xfc00
	s_waitcnt lgkmcnt(0)
	v_mfma_f32_32x32x16_bf16 v[50:65], v[66:69], v[82:85], v[50:65]
	ds_read_b64_tr_b16 v[82:83], v152 offset:0xc600
	ds_read_b64_tr_b16 v[84:85], v152 offset:0xce00
	v_mfma_f32_32x32x16_bf16 v[50:65], v[70:73], v[86:89], v[50:65]
	ds_read_b64_tr_b16 v[86:87], v152 offset:0xd600
	ds_read_b64_tr_b16 v[88:89], v152 offset:0xde00
	v_mfma_f32_32x32x16_bf16 v[50:65], v[74:77], v[90:93], v[50:65]
	ds_read_b64_tr_b16 v[90:91], v152 offset:0xe600
	ds_read_b64_tr_b16 v[92:93], v152 offset:0xee00
	v_mfma_f32_32x32x16_bf16 v[50:65], v[78:81], v[94:97], v[50:65]
	ds_read_b64_tr_b16 v[94:95], v152 offset:0xf600
	ds_read_b64_tr_b16 v[96:97], v152 offset:0xfe00
	s_waitcnt lgkmcnt(0)
	v_mfma_f32_32x32x16_bf16 v[2:17], v[66:69], v[82:85], v[2:17]
	v_mov_b32_e32 v145, v114
	v_mfma_f32_32x32x16_bf16 v[2:17], v[70:73], v[86:89], v[2:17]
	v_mfma_f32_32x32x16_bf16 v[2:17], v[74:77], v[90:93], v[2:17]
	v_mfma_f32_32x32x16_bf16 v[2:17], v[78:81], v[94:97], v[2:17]
	s_and_saveexec_b64 s[8:9], s[4:5]
	s_cbranch_execnz .LBB0_563
	s_branch .LBB0_564

; template <int DQK, int KB>
; __device__ __forceinline__ void qkt(f32x16& p0, f32x16& p1, const char* K_lds, int r32, int hi, const bf16x8* qr) {
;     constexpr int ROWB = DQK * 2, SHM_K = 64 * ROWB;
;     p0 = f32x16{}; p1 = f32x16{};
;     const char* kb[4];
; #pragma unroll
;     for (int dd = 0; dd < 4; ++dd) kb[dd] = K_lds + KB * SHM_K + r32 * ROWB + (((dd * 16 + hi * 8) * 2) ^ ((r32 & 7) << 4));
; #pragma unroll
;     for (int d0 = 0; d0 < DQK / 16; ++d0) { const char* a = kb[d0 & 3] + (d0 >> 2) * 128;
;         bf16x8 b0 = *reinterpret_cast<const bf16x8*>(a);
;         bf16x8 b1 = *reinterpret_cast<const bf16x8*>(a + 32 * ROWB);
;         p0 = __builtin_amdgcn_mfma_f32_32x32x16_bf16(b0, qr[d0], p0, 0, 0, 0);
;         p1 = __builtin_amdgcn_mfma_f32_32x32x16_bf16(b1, qr[d0], p1, 0, 0, 0); }
.LBB0_795:
	s_add_i32 s68, s78, 0xffffff80
	s_lshl_b64 s[4:5], s[68:69], 12
	s_add_u32 s4, s76, s4
	s_addc_u32 s5, s77, s5
	s_waitcnt vmcnt(2)
	v_lshl_add_u64 v[12:13], s[4:5], 0, v[174:175]
	v_add_co_u32_e32 v16, vcc, s96, v12
	v_lshl_add_u64 v[14:15], v[12:13], 0, s[72:73]
	s_nop 0
	v_addc_co_u32_e32 v17, vcc, 0, v13, vcc
	s_lshl_b64 s[4:5], s[68:69], 7
	global_load_dwordx4 v[4:7], v[12:13], off offset:256
	global_load_dwordx4 v[8:11], v[12:13], off
	s_nop 0
	global_load_dwordx4 v[12:15], v[14:15], off offset:256
	s_nop 0
	global_load_dwordx4 v[162:165], v[16:17], off
	v_lshl_add_u64 v[16:17], v[178:179], 0, s[4:5]
	global_load_dwordx4 v[166:169], v[16:17], off
	v_add_u32_e32 v2, v182, v183
	v_add_u32_e32 v16, v182, v184
	v_add_u32_e32 v207, v182, v185
	v_add_u32_e32 v208, v182, v186
	ds_read_b128 v[82:85], v2 offset:49152
	ds_read_b128 v[98:101], v2 offset:61440
	ds_read_b128 v[210:213], v16 offset:49152
	ds_read_b128 v[218:221], v16 offset:61440
	ds_read_b128 v[222:225], v207 offset:49152
	ds_read_b128 v[226:229], v207 offset:61440
	ds_read_b128 v[230:233], v208 offset:49152
	ds_read_b128 v[234:237], v208 offset:61440
	ds_read_b128 v[238:241], v2 offset:49280
	ds_read_b128 v[242:245], v2 offset:61568
	ds_read_b128 v[246:249], v16 offset:49280
	ds_read_b128 v[250:253], v16 offset:61568
	s_waitcnt lgkmcnt(10)
	v_mfma_f32_32x32x16_bf16 v[82:97], v[82:85], v[158:161], 0
	v_mfma_f32_32x32x16_bf16 v[98:113], v[98:101], v[158:161], 0
	s_waitcnt lgkmcnt(8)
	v_mfma_f32_32x32x16_bf16 v[82:97], v[210:213], v[154:157], v[82:97]
	ds_read_b128 v[210:213], v207 offset:49280
	v_mfma_f32_32x32x16_bf16 v[98:113], v[218:221], v[154:157], v[98:113]
	ds_read_b128 v[218:221], v207 offset:61568
	s_waitcnt lgkmcnt(8)
	v_mfma_f32_32x32x16_bf16 v[82:97], v[222:225], v[150:153], v[82:97]
	ds_read_b128 v[222:225], v208 offset:49280
	v_mfma_f32_32x32x16_bf16 v[98:113], v[226:229], v[150:153], v[98:113]
	ds_read_b128 v[226:229], v208 offset:61568
	s_waitcnt lgkmcnt(8)
	v_mfma_f32_32x32x16_bf16 v[82:97], v[230:233], v[142:145], v[82:97]
	ds_read_b128 v[230:233], v2 offset:49408
	v_mfma_f32_32x32x16_bf16 v[98:113], v[234:237], v[142:145], v[98:113]
	ds_read_b128 v[234:237], v2 offset:61696
	s_waitcnt lgkmcnt(8)
	v_mfma_f32_32x32x16_bf16 v[82:97], v[238:241], v[138:141], v[82:97]
	ds_read_b128 v[238:241], v16 offset:49408
	v_mfma_f32_32x32x16_bf16 v[98:113], v[242:245], v[138:141], v[98:113]
	ds_read_b128 v[242:245], v16 offset:61696
	s_waitcnt lgkmcnt(8)
	v_mfma_f32_32x32x16_bf16 v[82:97], v[246:249], v[134:137], v[82:97]
	ds_read_b128 v[246:249], v207 offset:49408
	v_mfma_f32_32x32x16_bf16 v[98:113], v[250:253], v[134:137], v[98:113]
	ds_read_b128 v[250:253], v207 offset:61696
	s_waitcnt lgkmcnt(8)
	v_mfma_f32_32x32x16_bf16 v[82:97], v[210:213], v[130:133], v[82:97]
	ds_read_b128 v[210:213], v208 offset:49408
	v_mfma_f32_32x32x16_bf16 v[98:113], v[218:221], v[130:133], v[98:113]
	ds_read_b128 v[218:221], v208 offset:61696
	s_waitcnt lgkmcnt(8)
	v_mfma_f32_32x32x16_bf16 v[82:97], v[222:225], v[126:129], v[82:97]
	v_mfma_f32_32x32x16_bf16 v[98:113], v[226:229], v[126:129], v[98:113]
	s_waitcnt lgkmcnt(6)
	v_mfma_f32_32x32x16_bf16 v[82:97], v[230:233], v[122:125], v[82:97]
	v_mfma_f32_32x32x16_bf16 v[98:113], v[234:237], v[122:125], v[98:113]
	s_waitcnt lgkmcnt(4)
	v_mfma_f32_32x32x16_bf16 v[82:97], v[238:241], v[118:121], v[82:97]
	v_mfma_f32_32x32x16_bf16 v[98:113], v[242:245], v[118:121], v[98:113]
	s_waitcnt lgkmcnt(2)
	v_mfma_f32_32x32x16_bf16 v[82:97], v[246:249], v[114:117], v[82:97]
	v_mfma_f32_32x32x16_bf16 v[98:113], v[250:253], v[114:117], v[98:113]
	s_add_i32 s4, s78, 0xffffff3f
	s_cmp_le_i32 s4, s84
	s_waitcnt lgkmcnt(1)
	v_mfma_f32_32x32x16_bf16 v[82:97], v[210:213], v[146:149], v[82:97]
	s_waitcnt lgkmcnt(0)
	v_mfma_f32_32x32x16_bf16 v[98:113], v[218:221], v[146:149], v[98:113]
	s_cbranch_scc1 .LBB0_797
; __device__ __forceinline__ void mask_tile(f32x16& p0, f32x16& p1, int dq) {
;     const float NEG = -__builtin_inff();
; #pragma unroll
;     for (int r = 0; r < 16; ++r) {
;         const int c = (r & 3) + 8 * (r >> 2);
;         if (dq - c < 0) p0[r] = NEG;
;         if (dq - c - 32 < 0) p1[r] = NEG;
;     }
; }
	v_cmp_gt_i32_e64 s[62:63], 26, v206
	v_cmp_gt_i32_e64 s[64:65], 27, v206
	v_cmp_gt_i32_e64 s[60:61], 25, v206
	s_and_b64 s[62:63], s[64:65], s[62:63]
	v_cmp_gt_i32_e64 s[58:59], 24, v206
	s_and_b64 s[60:61], s[62:63], s[60:61]
	v_cmp_gt_i32_e64 s[56:57], 19, v206
	s_and_b64 s[58:59], s[60:61], s[58:59]
	v_cmp_gt_i32_e64 s[54:55], 18, v206
	s_and_b64 s[56:57], s[58:59], s[56:57]
	v_cmp_gt_i32_e64 s[52:53], 17, v206
	s_and_b64 s[54:55], s[56:57], s[54:55]
	v_cmp_gt_i32_e64 s[50:51], 16, v206
	s_and_b64 s[52:53], s[54:55], s[52:53]
	v_cmp_gt_i32_e64 s[48:49], 11, v206
	s_and_b64 s[50:51], s[52:53], s[50:51]
	v_cmp_gt_i32_e64 s[46:47], 10, v206
	s_and_b64 s[48:49], s[50:51], s[48:49]
	v_cmp_gt_i32_e64 s[44:45], 9, v206
	s_and_b64 s[46:47], s[48:49], s[46:47]
	v_cmp_gt_i32_e64 s[42:43], 8, v206
	s_and_b64 s[44:45], s[46:47], s[44:45]
	v_cmp_gt_i32_e64 s[40:41], 3, v206
	s_and_b64 s[42:43], s[44:45], s[42:43]
	v_cmp_gt_i32_e64 s[38:39], 2, v206
	s_and_b64 s[40:41], s[42:43], s[40:41]
	v_cmp_gt_i32_e64 s[36:37], 1, v206
	s_and_b64 s[38:39], s[40:41], s[38:39]
	v_cmp_gt_i32_e64 s[34:35], 0, v206
	s_and_b64 s[36:37], s[38:39], s[36:37]
	s_and_b64 s[34:35], s[36:37], s[34:35]
	v_cmp_gt_i32_e64 s[30:31], 58, v206
	v_cndmask_b32_e64 v82, v82, v198, s[34:35]
	v_cmp_gt_i32_e64 s[34:35], 59, v206
	v_cmp_gt_i32_e64 s[28:29], 57, v206
	s_and_b64 s[30:31], s[34:35], s[30:31]
	v_cmp_gt_i32_e64 s[26:27], 56, v206
	s_and_b64 s[28:29], s[30:31], s[28:29]
	v_cmp_gt_i32_e64 s[24:25], 51, v206
	s_and_b64 s[26:27], s[28:29], s[26:27]
	v_cmp_gt_i32_e64 s[22:23], 50, v206
	s_and_b64 s[24:25], s[26:27], s[24:25]
	v_cmp_gt_i32_e64 s[20:21], 49, v206
	s_and_b64 s[22:23], s[24:25], s[22:23]
	v_cmp_gt_i32_e64 s[18:19], 48, v206
	s_and_b64 s[20:21], s[22:23], s[20:21]
	v_cmp_gt_i32_e64 s[16:17], 43, v206
	s_and_b64 s[18:19], s[20:21], s[18:19]
	v_cmp_gt_i32_e64 s[14:15], 42, v206
	s_and_b64 s[16:17], s[18:19], s[16:17]
	v_cmp_gt_i32_e64 s[12:13], 41, v206
	s_and_b64 s[14:15], s[16:17], s[14:15]
	v_cmp_gt_i32_e64 s[10:11], 40, v206
	s_and_b64 s[12:13], s[14:15], s[12:13]
	v_cmp_gt_i32_e64 s[8:9], 35, v206
	s_and_b64 s[10:11], s[12:13], s[10:11]
	v_cmp_gt_i32_e64 s[6:7], 34, v206
	s_and_b64 s[8:9], s[10:11], s[8:9]
	v_cmp_gt_i32_e64 s[4:5], 33, v206
	s_and_b64 s[6:7], s[8:9], s[6:7]
	v_cmp_gt_i32_e32 vcc, 32, v206
	s_and_b64 s[4:5], s[6:7], s[4:5]
	s_and_b64 vcc, s[4:5], vcc
	v_cndmask_b32_e64 v97, v97, v198, s[64:65]
	v_cndmask_b32_e64 v96, v96, v198, s[62:63]
	v_cndmask_b32_e64 v95, v95, v198, s[60:61]
	v_cndmask_b32_e64 v94, v94, v198, s[58:59]
	v_cndmask_b32_e64 v93, v93, v198, s[56:57]
	v_cndmask_b32_e64 v92, v92, v198, s[54:55]
	v_cndmask_b32_e64 v91, v91, v198, s[52:53]
	v_cndmask_b32_e64 v90, v90, v198, s[50:51]
	v_cndmask_b32_e64 v89, v89, v198, s[48:49]
	v_cndmask_b32_e64 v88, v88, v198, s[46:47]
	v_cndmask_b32_e64 v87, v87, v198, s[44:45]
	v_cndmask_b32_e64 v86, v86, v198, s[42:43]
	v_cndmask_b32_e64 v85, v85, v198, s[40:41]
	v_cndmask_b32_e64 v84, v84, v198, s[38:39]
	v_cndmask_b32_e64 v83, v83, v198, s[36:37]
	v_cndmask_b32_e64 v113, v113, v198, s[34:35]
	v_cndmask_b32_e64 v112, v112, v198, s[30:31]
	v_cndmask_b32_e64 v111, v111, v198, s[28:29]
	v_cndmask_b32_e64 v110, v110, v198, s[26:27]
	v_cndmask_b32_e64 v109, v109, v198, s[24:25]
	v_cndmask_b32_e64 v108, v108, v198, s[22:23]
	v_cndmask_b32_e64 v107, v107, v198, s[20:21]
	v_cndmask_b32_e64 v106, v106, v198, s[18:19]
	v_cndmask_b32_e64 v105, v105, v198, s[16:17]
	v_cndmask_b32_e64 v104, v104, v198, s[14:15]
	v_cndmask_b32_e64 v103, v103, v198, s[12:13]
	v_cndmask_b32_e64 v102, v102, v198, s[10:11]
	v_cndmask_b32_e64 v101, v101, v198, s[8:9]
	v_cndmask_b32_e64 v100, v100, v198, s[6:7]
	v_cndmask_b32_e64 v99, v99, v198, s[4:5]
	v_cndmask_b32_e32 v98, v98, v198, vcc

; template <int DQK> __device__ __forceinline__ void partialSM(f32x16& p0, f32x16& p1, float& m_reg, float& mn, float& alpha) {
;     ...
;     const float mnL = -mn * C2;
; #pragma unroll
;     for (int r = 0; r < 16; ++r) p0[r] = fmaf(p0[r], C2, mnL);
; #pragma unroll
;     for (int r = 0; r < 16; ++r) p1[r] = fmaf(p1[r], C2, mnL);
; #pragma unroll
;     for (int r = 0; r < 16; ++r) p0[r] = __builtin_amdgcn_exp2f(p0[r]);
; }
; __device__ __forceinline__ void finishSM(f32x16& p0, f32x16& p1, float alpha, float& l_reg, bf16x8& pa0, bf16x8& pa1, bf16x8& pa2, bf16x8& pa3) {
; #pragma unroll
;     for (int r = 0; r < 16; ++r) p1[r] = __builtin_amdgcn_exp2f(p1[r]);
;     float ps = 0;
; #pragma unroll
;     for (int r = 0; r < 16; ++r) ps += p0[r];
; #pragma unroll
;     for (int r = 0; r < 16; ++r) ps += p1[r];
;     { auto rr = __builtin_amdgcn_permlane32_swap(__float_as_uint(ps), __float_as_uint(ps), false, false);
;       ps = __uint_as_float(rr[0]) + __uint_as_float(rr[1]); }
;     l_reg = l_reg * alpha + ps;
;     ...
;     PK4(p0, 0, pa0); PK4(p0, 8, pa1); PK4(p1, 0, pa2); PK4(p1, 8, pa3);
; template <int VB>
; __device__ __forceinline__ void pv_tile(f32x16* o, int vb0, bf16x8 pa0, bf16x8 pa1, bf16x8 pa2, bf16x8 pa3) {
;     ...
;     PV_D0(0); PV_D0(1); PV_D0(2); PV_D0(3);
.LBB0_801:
	ds_read_b64_tr_b16 v[218:219], v181 offset:0
	ds_read_b64_tr_b16 v[220:221], v181 offset:2048
	ds_read_b64_tr_b16 v[222:223], v181 offset:4096
	ds_read_b64_tr_b16 v[224:225], v181 offset:6144
	ds_read_b64_tr_b16 v[226:227], v181 offset:8192
	ds_read_b64_tr_b16 v[228:229], v181 offset:10240
	ds_read_b64_tr_b16 v[230:231], v181 offset:12288
	ds_read_b64_tr_b16 v[232:233], v181 offset:14336
	ds_read_b64_tr_b16 v[234:235], v181 offset:512
	ds_read_b64_tr_b16 v[236:237], v181 offset:2560
	ds_read_b64_tr_b16 v[238:239], v181 offset:4608
	ds_read_b64_tr_b16 v[240:241], v181 offset:6656
	ds_read_b64_tr_b16 v[242:243], v181 offset:8704
	ds_read_b64_tr_b16 v[244:245], v181 offset:10752
	v_cndmask_b32_e64 v216, v216, v17, s[4:5]
	v_mul_f32_e32 v17, 0xbdd53b94, v216
	v_fmamk_f32 v82, v82, 0x3dd53b94, v17
	v_fmamk_f32 v83, v83, 0x3dd53b94, v17
	v_exp_f32_e32 v82, v82
	v_fmamk_f32 v84, v84, 0x3dd53b94, v17
	v_exp_f32_e32 v83, v83
	v_fmamk_f32 v85, v85, 0x3dd53b94, v17
	v_exp_f32_e32 v84, v84
	v_fmamk_f32 v86, v86, 0x3dd53b94, v17
	v_exp_f32_e32 v85, v85
	v_fmamk_f32 v87, v87, 0x3dd53b94, v17
	v_fmamk_f32 v88, v88, 0x3dd53b94, v17
	v_fmamk_f32 v89, v89, 0x3dd53b94, v17
	v_fmamk_f32 v90, v90, 0x3dd53b94, v17
	v_fmamk_f32 v91, v91, 0x3dd53b94, v17
	v_fmamk_f32 v92, v92, 0x3dd53b94, v17
	v_fmamk_f32 v93, v93, 0x3dd53b94, v17
	v_fmamk_f32 v94, v94, 0x3dd53b94, v17
	v_fmamk_f32 v95, v95, 0x3dd53b94, v17
	v_fmamk_f32 v96, v96, 0x3dd53b94, v17
	v_fmamk_f32 v97, v97, 0x3dd53b94, v17
	v_fmamk_f32 v98, v98, 0x3dd53b94, v17
	v_fmamk_f32 v99, v99, 0x3dd53b94, v17
	v_fmamk_f32 v100, v100, 0x3dd53b94, v17
	v_fmamk_f32 v101, v101, 0x3dd53b94, v17
	v_fmamk_f32 v102, v102, 0x3dd53b94, v17
	v_fmamk_f32 v103, v103, 0x3dd53b94, v17
	v_fmamk_f32 v104, v104, 0x3dd53b94, v17
	v_fmamk_f32 v105, v105, 0x3dd53b94, v17
	v_fmamk_f32 v106, v106, 0x3dd53b94, v17
	v_fmamk_f32 v107, v107, 0x3dd53b94, v17
	v_fmamk_f32 v108, v108, 0x3dd53b94, v17
	v_fmamk_f32 v109, v109, 0x3dd53b94, v17
	v_fmamk_f32 v110, v110, 0x3dd53b94, v17
	v_fmamk_f32 v111, v111, 0x3dd53b94, v17
	v_fmamk_f32 v112, v112, 0x3dd53b94, v17
	v_fmac_f32_e32 v17, 0x3dd53b94, v113
	v_exp_f32_e32 v86, v86
	v_add_f32_e32 v113, 0, v82
	v_exp_f32_e32 v87, v87
	v_add_f32_e32 v113, v83, v113
	v_exp_f32_e32 v88, v88
	v_add_f32_e32 v113, v84, v113
	v_exp_f32_e32 v89, v89
	v_add_f32_e32 v113, v85, v113
	v_exp_f32_e32 v90, v90
	v_add_f32_e32 v113, v86, v113
	v_exp_f32_e32 v91, v91
	v_add_f32_e32 v113, v87, v113
	v_exp_f32_e32 v92, v92
	v_add_f32_e32 v113, v88, v113
	v_exp_f32_e32 v93, v93
	v_add_f32_e32 v113, v89, v113
	v_exp_f32_e32 v94, v94
	v_add_f32_e32 v113, v90, v113
	v_exp_f32_e32 v95, v95
	v_add_f32_e32 v113, v91, v113
	v_exp_f32_e32 v96, v96
	v_add_f32_e32 v113, v92, v113
	v_exp_f32_e32 v97, v97
	v_add_f32_e32 v113, v93, v113
	v_exp_f32_e32 v98, v98
	v_add_f32_e32 v113, v94, v113
	v_exp_f32_e32 v99, v99
	v_add_f32_e32 v113, v95, v113
	v_exp_f32_e32 v100, v100
	v_add_f32_e32 v113, v96, v113
	v_exp_f32_e32 v101, v101
	v_add_f32_e32 v113, v97, v113
	v_exp_f32_e32 v102, v102
	v_add_f32_e32 v113, v98, v113
	v_exp_f32_e32 v103, v103
	v_add_f32_e32 v113, v99, v113
	v_exp_f32_e32 v104, v104
	v_add_f32_e32 v113, v100, v113
	v_exp_f32_e32 v105, v105
	v_add_f32_e32 v113, v101, v113
	v_exp_f32_e32 v106, v106
	v_add_f32_e32 v113, v102, v113
	v_exp_f32_e32 v107, v107
	v_add_f32_e32 v113, v103, v113
	v_exp_f32_e32 v108, v108
	v_add_f32_e32 v113, v104, v113
	v_exp_f32_e32 v109, v109
	v_add_f32_e32 v113, v105, v113
	v_exp_f32_e32 v110, v110
	v_add_f32_e32 v113, v106, v113
	v_exp_f32_e32 v111, v111
	v_add_f32_e32 v113, v107, v113
	v_exp_f32_e32 v112, v112
	v_add_f32_e32 v113, v108, v113
	v_exp_f32_e32 v17, v17
	v_add_f32_e32 v113, v109, v113
	v_add_f32_e32 v113, v110, v113
	v_add_f32_e32 v113, v111, v113
	v_add_f32_e32 v113, v112, v113
	v_add_f32_e32 v213, v17, v113
	v_mov_b32_e32 v214, v213
	s_nop 1
	v_permlane32_swap_b32_e32 v213, v214
	v_cvt_pk_bf16_f32 v82, v82, v83
	v_cvt_pk_bf16_f32 v83, v84, v85
	v_cvt_pk_bf16_f32 v84, v86, v87
	v_cvt_pk_bf16_f32 v85, v88, v89
	v_cvt_pk_bf16_f32 v86, v90, v91
	v_cvt_pk_bf16_f32 v87, v92, v93
	v_cvt_pk_bf16_f32 v88, v94, v95
	v_cvt_pk_bf16_f32 v89, v96, v97
	v_cvt_pk_bf16_f32 v90, v98, v99
	v_cvt_pk_bf16_f32 v91, v100, v101
	v_cvt_pk_bf16_f32 v92, v102, v103
	v_cvt_pk_bf16_f32 v93, v104, v105
	v_cvt_pk_bf16_f32 v94, v106, v107
	v_cvt_pk_bf16_f32 v95, v108, v109
	v_cvt_pk_bf16_f32 v96, v110, v111
	v_cvt_pk_bf16_f32 v97, v112, v17
	s_nop 0
	v_permlane32_swap_b32_e32 v82, v84
	v_permlane32_swap_b32_e32 v83, v85
	v_permlane32_swap_b32_e32 v86, v88
	v_permlane32_swap_b32_e32 v87, v89
	v_permlane32_swap_b32_e32 v90, v92
	v_permlane32_swap_b32_e32 v91, v93
	v_permlane32_swap_b32_e32 v94, v96
	v_permlane32_swap_b32_e32 v95, v97
	s_waitcnt lgkmcnt(0)
	ds_read_b64_tr_b16 v[246:247], v181 offset:12800
	ds_read_b64_tr_b16 v[248:249], v181 offset:14848
	ds_read_b64_tr_b16 v[250:251], v181 offset:1024
	ds_read_b64_tr_b16 v[252:253], v181 offset:3072
	ds_read_b64_tr_b16 v[98:99], v181 offset:5120
	ds_read_b64_tr_b16 v[100:101], v181 offset:7168
	ds_read_b64_tr_b16 v[102:103], v181 offset:9216
	ds_read_b64_tr_b16 v[104:105], v181 offset:11264
	ds_read_b64_tr_b16 v[106:107], v181 offset:13312
	ds_read_b64_tr_b16 v[108:109], v181 offset:15360
	ds_read_b64_tr_b16 v[110:111], v181 offset:1536
	ds_read_b64_tr_b16 v[112:113], v181 offset:3584
	v_mfma_f32_32x32x16_bf16 v[66:81], v[82:85], v[218:221], v[66:81]
	ds_read_b64_tr_b16 v[218:219], v181 offset:5632
	ds_read_b64_tr_b16 v[220:221], v181 offset:7680
	v_mfma_f32_32x32x16_bf16 v[66:81], v[86:89], v[222:225], v[66:81]
	s_waitcnt lgkmcnt(13)
	ds_read_b64_tr_b16 v[222:223], v181 offset:9728
	ds_read_b64_tr_b16 v[224:225], v181 offset:11776
	v_mfma_f32_32x32x16_bf16 v[66:81], v[90:93], v[226:229], v[66:81]
	s_waitcnt lgkmcnt(13)
	ds_read_b64_tr_b16 v[226:227], v181 offset:13824
	ds_read_b64_tr_b16 v[228:229], v181 offset:15872
	v_mfma_f32_32x32x16_bf16 v[66:81], v[94:97], v[230:233], v[66:81]
	v_mfma_f32_32x32x16_bf16 v[50:65], v[82:85], v[234:237], v[50:65]
	v_mfma_f32_32x32x16_bf16 v[50:65], v[86:89], v[238:241], v[50:65]
	s_waitcnt lgkmcnt(15)
	v_mfma_f32_32x32x16_bf16 v[50:65], v[90:93], v[242:245], v[50:65]
	v_mfma_f32_32x32x16_bf16 v[50:65], v[94:97], v[246:249], v[50:65]
	s_waitcnt lgkmcnt(12)
	v_mfma_f32_32x32x16_bf16 v[34:49], v[82:85], v[250:253], v[34:49]
	v_mfma_f32_32x32x16_bf16 v[34:49], v[86:89], v[98:101], v[34:49]
	s_waitcnt lgkmcnt(8)
	v_mfma_f32_32x32x16_bf16 v[34:49], v[90:93], v[102:105], v[34:49]
	v_mfma_f32_32x32x16_bf16 v[34:49], v[94:97], v[106:109], v[34:49]
	s_waitcnt lgkmcnt(6)
	v_mfma_f32_32x32x16_bf16 v[18:33], v[82:85], v[110:113], v[18:33]
	v_add_u32_e32 v17, s33, v173
	s_waitcnt vmcnt(3)
	ds_write_b128 v17, v[8:11]
	s_waitcnt vmcnt(1)
	ds_write_b128 v17, v[162:165] offset:12288
	v_add_u32_e32 v17, s33, v180
	s_waitcnt vmcnt(0)
	ds_write_b128 v17, v[166:169]
	ds_write_b128 v194, v[4:7] offset:32768
	ds_write_b128 v195, v[12:15] offset:32768
	s_waitcnt lgkmcnt(0)
	s_barrier
	v_mfma_f32_32x32x16_bf16 v[18:33], v[86:89], v[218:221], v[18:33]
	s_add_i32 s4, s86, 6
	s_cmp_lt_u32 s4, s85
	s_cselect_b64 s[66:67], -1, 0
	s_cmp_ge_u32 s4, s85
	v_mfma_f32_32x32x16_bf16 v[18:33], v[90:93], v[222:225], v[18:33]
	v_mfma_f32_32x32x16_bf16 v[18:33], v[94:97], v[226:229], v[18:33]
	s_cbranch_scc1 .LBB0_803
	s_sub_i32 s4, s78, 64
	s_ashr_i32 s5, s4, 31
	s_lshl_b64 s[6:7], s[4:5], 12
	s_add_u32 s6, s76, s6
	s_addc_u32 s7, s77, s7
	v_lshl_add_u64 v[12:13], s[6:7], 0, v[174:175]
	v_add_co_u32_e32 v82, vcc, 0x20000, v12
	v_lshl_add_u64 v[14:15], v[12:13], 0, s[72:73]
	s_nop 0
	v_addc_co_u32_e32 v83, vcc, 0, v13, vcc
	s_lshl_b64 s[4:5], s[4:5], 7
	global_load_dwordx4 v[4:7], v[12:13], off offset:256
	global_load_dwordx4 v[8:11], v[12:13], off
	s_nop 0
	global_load_dwordx4 v[12:15], v[14:15], off offset:256
	s_nop 0
	global_load_dwordx4 v[162:165], v[82:83], off
	v_lshl_add_u64 v[82:83], v[178:179], 0, s[4:5]
	global_load_dwordx4 v[166:169], v[82:83], off
; __device__ __forceinline__ void mask_tile(f32x16& p0, f32x16& p1, int dq) {
;     const float NEG = -__builtin_inff();
; #pragma unroll
;     for (int r = 0; r < 16; ++r) {
;         const int c = (r & 3) + 8 * (r >> 2);
;         if (dq - c < 0) p0[r] = NEG;
;         if (dq - c - 32 < 0) p1[r] = NEG;
;     }
; }
; template <int DQK, int KB>
; __device__ __forceinline__ void qkt(f32x16& p0, f32x16& p1, const char* K_lds, int r32, int hi, const bf16x8* qr) {
;     constexpr int ROWB = DQK * 2, SHM_K = 64 * ROWB;
;     p0 = f32x16{}; p1 = f32x16{};
;     const char* kb[4];
; #pragma unroll
;     for (int dd = 0; dd < 4; ++dd) kb[dd] = K_lds + KB * SHM_K + r32 * ROWB + (((dd * 16 + hi * 8) * 2) ^ ((r32 & 7) << 4));
; #pragma unroll
;     for (int d0 = 0; d0 < DQK / 16; ++d0) { const char* a = kb[d0 & 3] + (d0 >> 2) * 128;
;         bf16x8 b0 = *reinterpret_cast<const bf16x8*>(a);
;         bf16x8 b1 = *reinterpret_cast<const bf16x8*>(a + 32 * ROWB);
;         p0 = __builtin_amdgcn_mfma_f32_32x32x16_bf16(b0, qr[d0], p0, 0, 0, 0);
;         p1 = __builtin_amdgcn_mfma_f32_32x32x16_bf16(b1, qr[d0], p1, 0, 0, 0); }
.LBB0_803:
	v_add_u32_e32 v17, v188, v183
	v_add_u32_e32 v209, v188, v184
	v_add_u32_e32 v210, v188, v185
	v_add_u32_e32 v211, v188, v186
	ds_read_b128 v[82:85], v17
	ds_read_b128 v[98:101], v17 offset:12288
	ds_read_b128 v[218:221], v209
	ds_read_b128 v[222:225], v209 offset:12288
	ds_read_b128 v[226:229], v210
	ds_read_b128 v[230:233], v210 offset:12288
	ds_read_b128 v[234:237], v211
	ds_read_b128 v[238:241], v211 offset:12288
	ds_read_b128 v[242:245], v17 offset:128
	ds_read_b128 v[246:249], v17 offset:12416
	ds_read_b128 v[250:253], v209 offset:128
	s_waitcnt lgkmcnt(9)
	v_mfma_f32_32x32x16_bf16 v[82:97], v[82:85], v[158:161], 0
	v_mfma_f32_32x32x16_bf16 v[98:113], v[98:101], v[158:161], 0
	s_waitcnt lgkmcnt(7)
	v_mfma_f32_32x32x16_bf16 v[82:97], v[218:221], v[154:157], v[82:97]
	ds_read_b128 v[218:221], v209 offset:12416
	v_mfma_f32_32x32x16_bf16 v[98:113], v[222:225], v[154:157], v[98:113]
	ds_read_b128 v[222:225], v210 offset:128
	s_waitcnt lgkmcnt(7)
	v_mfma_f32_32x32x16_bf16 v[82:97], v[226:229], v[150:153], v[82:97]
	ds_read_b128 v[226:229], v210 offset:12416
	v_mfma_f32_32x32x16_bf16 v[98:113], v[230:233], v[150:153], v[98:113]
	ds_read_b128 v[230:233], v211 offset:128
	s_waitcnt lgkmcnt(7)
	v_mfma_f32_32x32x16_bf16 v[82:97], v[234:237], v[142:145], v[82:97]
	ds_read_b128 v[234:237], v211 offset:12416
	v_mfma_f32_32x32x16_bf16 v[98:113], v[238:241], v[142:145], v[98:113]
	ds_read_b128 v[238:241], v17 offset:256
	s_waitcnt lgkmcnt(7)
	v_mfma_f32_32x32x16_bf16 v[82:97], v[242:245], v[138:141], v[82:97]
	ds_read_b128 v[242:245], v17 offset:12544
	v_mfma_f32_32x32x16_bf16 v[98:113], v[246:249], v[138:141], v[98:113]
	ds_read_b128 v[246:249], v209 offset:256
	s_waitcnt lgkmcnt(7)
	v_mfma_f32_32x32x16_bf16 v[82:97], v[250:253], v[134:137], v[82:97]
	ds_read_b128 v[250:253], v209 offset:12544
	v_mfma_f32_32x32x16_bf16 v[98:113], v[218:221], v[134:137], v[98:113]
	ds_read_b128 v[218:221], v210 offset:256
	s_waitcnt lgkmcnt(7)
	v_mfma_f32_32x32x16_bf16 v[82:97], v[222:225], v[130:133], v[82:97]
	ds_read_b128 v[222:225], v210 offset:12544
	v_mfma_f32_32x32x16_bf16 v[98:113], v[226:229], v[130:133], v[98:113]
	ds_read_b128 v[226:229], v211 offset:256
	s_waitcnt lgkmcnt(7)
	v_mfma_f32_32x32x16_bf16 v[82:97], v[230:233], v[126:129], v[82:97]
	ds_read_b128 v[230:233], v211 offset:12544
	v_mfma_f32_32x32x16_bf16 v[98:113], v[234:237], v[126:129], v[98:113]
	s_waitcnt lgkmcnt(6)
	v_mfma_f32_32x32x16_bf16 v[82:97], v[238:241], v[122:125], v[82:97]
	v_mfma_f32_32x32x16_bf16 v[98:113], v[242:245], v[122:125], v[98:113]
	s_waitcnt lgkmcnt(4)
	v_mfma_f32_32x32x16_bf16 v[82:97], v[246:249], v[118:121], v[82:97]
	v_mfma_f32_32x32x16_bf16 v[98:113], v[250:253], v[118:121], v[98:113]
	s_waitcnt lgkmcnt(2)
	v_mfma_f32_32x32x16_bf16 v[82:97], v[218:221], v[114:117], v[82:97]
	v_mfma_f32_32x32x16_bf16 v[98:113], v[222:225], v[114:117], v[98:113]
	s_add_i32 s4, s78, 0xffffff7f
	s_cmp_le_i32 s4, s84
	s_waitcnt lgkmcnt(1)
	v_mfma_f32_32x32x16_bf16 v[82:97], v[226:229], v[146:149], v[82:97]
	s_waitcnt lgkmcnt(0)
	v_mfma_f32_32x32x16_bf16 v[98:113], v[230:233], v[146:149], v[98:113]
	s_cbranch_scc1 .LBB0_805
	v_subrev_u32_e32 v215, 64, v206
	v_cmp_gt_i32_e64 s[62:63], 26, v215
	v_cmp_gt_i32_e64 s[64:65], 27, v215
	v_cmp_gt_i32_e64 s[60:61], 25, v215
	s_and_b64 s[62:63], s[64:65], s[62:63]
	v_cmp_gt_i32_e64 s[58:59], 24, v215
	s_and_b64 s[60:61], s[62:63], s[60:61]
	v_cmp_gt_i32_e64 s[56:57], 19, v215
	s_and_b64 s[58:59], s[60:61], s[58:59]
	v_cmp_gt_i32_e64 s[54:55], 18, v215
	s_and_b64 s[56:57], s[58:59], s[56:57]
	v_cmp_gt_i32_e64 s[52:53], 17, v215
	s_and_b64 s[54:55], s[56:57], s[54:55]
	v_cmp_gt_i32_e64 s[50:51], 16, v215
	s_and_b64 s[52:53], s[54:55], s[52:53]
	v_cmp_gt_i32_e64 s[48:49], 11, v215
	s_and_b64 s[50:51], s[52:53], s[50:51]
	v_cmp_gt_i32_e64 s[46:47], 10, v215
	s_and_b64 s[48:49], s[50:51], s[48:49]
	v_cmp_gt_i32_e64 s[44:45], 9, v215
	s_and_b64 s[46:47], s[48:49], s[46:47]
	v_cmp_gt_i32_e64 s[42:43], 8, v215
	s_and_b64 s[44:45], s[46:47], s[44:45]
	v_cmp_gt_i32_e64 s[40:41], 3, v215
	s_and_b64 s[42:43], s[44:45], s[42:43]
	v_cmp_gt_i32_e64 s[38:39], 2, v215
	s_and_b64 s[40:41], s[42:43], s[40:41]
	v_cmp_gt_i32_e64 s[36:37], 1, v215
	s_and_b64 s[38:39], s[40:41], s[38:39]
	v_cmp_gt_i32_e64 s[34:35], 0, v215
	s_and_b64 s[36:37], s[38:39], s[36:37]
	s_and_b64 s[34:35], s[36:37], s[34:35]
	v_cmp_gt_i32_e64 s[30:31], 58, v215
	v_cndmask_b32_e64 v82, v82, v198, s[34:35]
	v_cmp_gt_i32_e64 s[34:35], 59, v215
	v_cmp_gt_i32_e64 s[28:29], 57, v215
	s_and_b64 s[30:31], s[34:35], s[30:31]
	v_cmp_gt_i32_e64 s[26:27], 56, v215
	s_and_b64 s[28:29], s[30:31], s[28:29]
	v_cmp_gt_i32_e64 s[24:25], 51, v215
	s_and_b64 s[26:27], s[28:29], s[26:27]
	v_cmp_gt_i32_e64 s[22:23], 50, v215
	s_and_b64 s[24:25], s[26:27], s[24:25]
	v_cmp_gt_i32_e64 s[20:21], 49, v215
	s_and_b64 s[22:23], s[24:25], s[22:23]
	v_cmp_gt_i32_e64 s[18:19], 48, v215
	s_and_b64 s[20:21], s[22:23], s[20:21]
	v_cmp_gt_i32_e64 s[16:17], 43, v215
	s_and_b64 s[18:19], s[20:21], s[18:19]
	v_cmp_gt_i32_e64 s[14:15], 42, v215
	s_and_b64 s[16:17], s[18:19], s[16:17]
	v_cmp_gt_i32_e64 s[12:13], 41, v215
	s_and_b64 s[14:15], s[16:17], s[14:15]
	v_cmp_gt_i32_e64 s[10:11], 40, v215
	s_and_b64 s[12:13], s[14:15], s[12:13]
	v_cmp_gt_i32_e64 s[8:9], 35, v215
	s_and_b64 s[10:11], s[12:13], s[10:11]
	v_cmp_gt_i32_e64 s[6:7], 34, v215
	s_and_b64 s[8:9], s[10:11], s[8:9]
	v_cmp_gt_i32_e64 s[4:5], 33, v215
	s_and_b64 s[6:7], s[8:9], s[6:7]
	v_cmp_gt_i32_e32 vcc, 32, v215
	s_and_b64 s[4:5], s[6:7], s[4:5]
	s_and_b64 vcc, s[4:5], vcc
	v_cndmask_b32_e64 v97, v97, v198, s[64:65]
	v_cndmask_b32_e64 v96, v96, v198, s[62:63]
	v_cndmask_b32_e64 v95, v95, v198, s[60:61]
	v_cndmask_b32_e64 v94, v94, v198, s[58:59]
	v_cndmask_b32_e64 v93, v93, v198, s[56:57]
	v_cndmask_b32_e64 v92, v92, v198, s[54:55]
	v_cndmask_b32_e64 v91, v91, v198, s[52:53]
	v_cndmask_b32_e64 v90, v90, v198, s[50:51]
	v_cndmask_b32_e64 v89, v89, v198, s[48:49]
	v_cndmask_b32_e64 v88, v88, v198, s[46:47]
	v_cndmask_b32_e64 v87, v87, v198, s[44:45]
	v_cndmask_b32_e64 v86, v86, v198, s[42:43]
	v_cndmask_b32_e64 v85, v85, v198, s[40:41]
	v_cndmask_b32_e64 v84, v84, v198, s[38:39]
	v_cndmask_b32_e64 v83, v83, v198, s[36:37]
	v_cndmask_b32_e64 v113, v113, v198, s[34:35]
	v_cndmask_b32_e64 v112, v112, v198, s[30:31]
	v_cndmask_b32_e64 v111, v111, v198, s[28:29]
	v_cndmask_b32_e64 v110, v110, v198, s[26:27]
	v_cndmask_b32_e64 v109, v109, v198, s[24:25]
	v_cndmask_b32_e64 v108, v108, v198, s[22:23]
	v_cndmask_b32_e64 v107, v107, v198, s[20:21]
	v_cndmask_b32_e64 v106, v106, v198, s[18:19]
	v_cndmask_b32_e64 v105, v105, v198, s[16:17]
	v_cndmask_b32_e64 v104, v104, v198, s[14:15]
	v_cndmask_b32_e64 v103, v103, v198, s[12:13]
	v_cndmask_b32_e64 v102, v102, v198, s[10:11]
	v_cndmask_b32_e64 v101, v101, v198, s[8:9]
	v_cndmask_b32_e64 v100, v100, v198, s[6:7]
	v_cndmask_b32_e64 v99, v99, v198, s[4:5]
	v_cndmask_b32_e32 v98, v98, v198, vcc

; template <int DQK> __device__ __forceinline__ void partialSM(f32x16& p0, f32x16& p1, float& m_reg, float& mn, float& alpha) {
;     ...
;     const float mnL = -mn * C2;
; #pragma unroll
;     for (int r = 0; r < 16; ++r) p0[r] = fmaf(p0[r], C2, mnL);
; #pragma unroll
;     for (int r = 0; r < 16; ++r) p1[r] = fmaf(p1[r], C2, mnL);
; #pragma unroll
;     for (int r = 0; r < 16; ++r) p0[r] = __builtin_amdgcn_exp2f(p0[r]);
; }
; __device__ __forceinline__ void finishSM(f32x16& p0, f32x16& p1, float alpha, float& l_reg, bf16x8& pa0, bf16x8& pa1, bf16x8& pa2, bf16x8& pa3) {
; #pragma unroll
;     for (int r = 0; r < 16; ++r) p1[r] = __builtin_amdgcn_exp2f(p1[r]);
;     float ps = 0;
; #pragma unroll
;     for (int r = 0; r < 16; ++r) ps += p0[r];
; #pragma unroll
;     for (int r = 0; r < 16; ++r) ps += p1[r];
;     { auto rr = __builtin_amdgcn_permlane32_swap(__float_as_uint(ps), __float_as_uint(ps), false, false);
;       ps = __uint_as_float(rr[0]) + __uint_as_float(rr[1]); }
;     l_reg = l_reg * alpha + ps;
;     ...
;     PK4(p0, 0, pa0); PK4(p0, 8, pa1); PK4(p1, 0, pa2); PK4(p1, 8, pa3);
; template <int VB>
; __device__ __forceinline__ void pv_tile(f32x16* o, int vb0, bf16x8 pa0, bf16x8 pa1, bf16x8 pa2, bf16x8 pa3) {
;     ...
;     PV_D0(0); PV_D0(1); PV_D0(2); PV_D0(3);
.LBB0_809:
	ds_read_b64_tr_b16 v[220:221], v181 offset:16384
	ds_read_b64_tr_b16 v[222:223], v181 offset:18432
	ds_read_b64_tr_b16 v[224:225], v181 offset:20480
	ds_read_b64_tr_b16 v[226:227], v181 offset:22528
	ds_read_b64_tr_b16 v[228:229], v181 offset:24576
	ds_read_b64_tr_b16 v[230:231], v181 offset:26624
	ds_read_b64_tr_b16 v[232:233], v181 offset:28672
	ds_read_b64_tr_b16 v[234:235], v181 offset:30720
	ds_read_b64_tr_b16 v[236:237], v181 offset:16896
	ds_read_b64_tr_b16 v[238:239], v181 offset:18944
	ds_read_b64_tr_b16 v[240:241], v181 offset:20992
	ds_read_b64_tr_b16 v[242:243], v181 offset:23040
	ds_read_b64_tr_b16 v[244:245], v181 offset:25088
	ds_read_b64_tr_b16 v[246:247], v181 offset:27136
	v_cndmask_b32_e64 v216, v216, v217, s[4:5]
	v_mul_f32_e32 v217, 0xbdd53b94, v216
	v_fmamk_f32 v82, v82, 0x3dd53b94, v217
	v_fmamk_f32 v83, v83, 0x3dd53b94, v217
	v_exp_f32_e32 v82, v82
	v_fmamk_f32 v84, v84, 0x3dd53b94, v217
	v_exp_f32_e32 v83, v83
	v_fmamk_f32 v85, v85, 0x3dd53b94, v217
	v_exp_f32_e32 v84, v84
	v_fmamk_f32 v86, v86, 0x3dd53b94, v217
	v_fmamk_f32 v87, v87, 0x3dd53b94, v217
	v_fmamk_f32 v88, v88, 0x3dd53b94, v217
	v_fmamk_f32 v89, v89, 0x3dd53b94, v217
	v_fmamk_f32 v90, v90, 0x3dd53b94, v217
	v_fmamk_f32 v91, v91, 0x3dd53b94, v217
	v_fmamk_f32 v92, v92, 0x3dd53b94, v217
	v_fmamk_f32 v93, v93, 0x3dd53b94, v217
	v_fmamk_f32 v94, v94, 0x3dd53b94, v217
	v_fmamk_f32 v95, v95, 0x3dd53b94, v217
	v_fmamk_f32 v96, v96, 0x3dd53b94, v217
	v_fmamk_f32 v97, v97, 0x3dd53b94, v217
	v_fmamk_f32 v98, v98, 0x3dd53b94, v217
	v_fmamk_f32 v99, v99, 0x3dd53b94, v217
	v_fmamk_f32 v100, v100, 0x3dd53b94, v217
	v_fmamk_f32 v101, v101, 0x3dd53b94, v217
	v_fmamk_f32 v102, v102, 0x3dd53b94, v217
	v_fmamk_f32 v103, v103, 0x3dd53b94, v217
	v_fmamk_f32 v104, v104, 0x3dd53b94, v217
	v_fmamk_f32 v105, v105, 0x3dd53b94, v217
	v_fmamk_f32 v106, v106, 0x3dd53b94, v217
	v_fmamk_f32 v107, v107, 0x3dd53b94, v217
	v_fmamk_f32 v108, v108, 0x3dd53b94, v217
	v_fmamk_f32 v109, v109, 0x3dd53b94, v217
	v_fmamk_f32 v110, v110, 0x3dd53b94, v217
	v_fmamk_f32 v111, v111, 0x3dd53b94, v217
	v_fmamk_f32 v112, v112, 0x3dd53b94, v217
	v_fmac_f32_e32 v217, 0x3dd53b94, v113
	v_exp_f32_e32 v85, v85
	v_exp_f32_e32 v86, v86
	v_exp_f32_e32 v113, v217
	v_add_f32_e32 v217, 0, v82
	v_exp_f32_e32 v87, v87
	v_add_f32_e32 v217, v83, v217
	v_exp_f32_e32 v88, v88
	v_add_f32_e32 v217, v84, v217
	v_exp_f32_e32 v89, v89
	v_add_f32_e32 v217, v85, v217
	v_exp_f32_e32 v90, v90
	v_add_f32_e32 v217, v86, v217
	v_exp_f32_e32 v91, v91
	v_add_f32_e32 v217, v87, v217
	v_exp_f32_e32 v92, v92
	v_add_f32_e32 v217, v88, v217
	v_exp_f32_e32 v93, v93
	v_add_f32_e32 v217, v89, v217
	v_exp_f32_e32 v94, v94
	v_add_f32_e32 v217, v90, v217
	v_exp_f32_e32 v95, v95
	v_add_f32_e32 v217, v91, v217
	v_exp_f32_e32 v96, v96
	v_add_f32_e32 v217, v92, v217
	v_exp_f32_e32 v97, v97
	v_add_f32_e32 v217, v93, v217
	v_exp_f32_e32 v98, v98
	v_add_f32_e32 v217, v94, v217
	v_exp_f32_e32 v99, v99
	v_add_f32_e32 v217, v95, v217
	v_exp_f32_e32 v100, v100
	v_add_f32_e32 v217, v96, v217
	v_exp_f32_e32 v101, v101
	v_add_f32_e32 v217, v97, v217
	v_exp_f32_e32 v102, v102
	v_add_f32_e32 v217, v98, v217
	v_exp_f32_e32 v103, v103
	v_add_f32_e32 v217, v99, v217
	v_exp_f32_e32 v104, v104
	v_add_f32_e32 v217, v100, v217
	v_exp_f32_e32 v105, v105
	v_add_f32_e32 v217, v101, v217
	v_exp_f32_e32 v106, v106
	v_add_f32_e32 v217, v102, v217
	v_exp_f32_e32 v107, v107
	v_add_f32_e32 v217, v103, v217
	v_exp_f32_e32 v108, v108
	v_add_f32_e32 v217, v104, v217
	v_exp_f32_e32 v109, v109
	v_add_f32_e32 v217, v105, v217
	v_exp_f32_e32 v110, v110
	v_add_f32_e32 v217, v106, v217
	v_exp_f32_e32 v111, v111
	v_add_f32_e32 v217, v107, v217
	v_exp_f32_e32 v112, v112
	v_add_f32_e32 v217, v108, v217
	v_add_f32_e32 v217, v109, v217
	v_add_f32_e32 v217, v110, v217
	v_add_f32_e32 v217, v111, v217
	v_add_f32_e32 v217, v112, v217
	v_add_f32_e32 v217, v113, v217
	v_mov_b32_e32 v218, v217
	s_nop 1
	v_permlane32_swap_b32_e32 v217, v218
	v_cvt_pk_bf16_f32 v82, v82, v83
	v_cvt_pk_bf16_f32 v83, v84, v85
	v_cvt_pk_bf16_f32 v84, v86, v87
	v_cvt_pk_bf16_f32 v85, v88, v89
	v_cvt_pk_bf16_f32 v86, v90, v91
	v_cvt_pk_bf16_f32 v87, v92, v93
	v_cvt_pk_bf16_f32 v88, v94, v95
	v_cvt_pk_bf16_f32 v89, v96, v97
	v_cvt_pk_bf16_f32 v90, v98, v99
	v_cvt_pk_bf16_f32 v91, v100, v101
	v_cvt_pk_bf16_f32 v92, v102, v103
	v_cvt_pk_bf16_f32 v93, v104, v105
	v_cvt_pk_bf16_f32 v94, v106, v107
	v_cvt_pk_bf16_f32 v95, v108, v109
	v_cvt_pk_bf16_f32 v96, v110, v111
	v_cvt_pk_bf16_f32 v97, v112, v113
	s_nop 0
	v_permlane32_swap_b32_e32 v82, v84
	v_permlane32_swap_b32_e32 v83, v85
	v_permlane32_swap_b32_e32 v86, v88
	v_permlane32_swap_b32_e32 v87, v89
	v_permlane32_swap_b32_e32 v90, v92
	v_permlane32_swap_b32_e32 v91, v93
	v_permlane32_swap_b32_e32 v94, v96
	v_permlane32_swap_b32_e32 v95, v97
	s_waitcnt lgkmcnt(0)
; template <int VB>
; __device__ __forceinline__ void pv_tile(f32x16* o, int vb0, bf16x8 pa0, bf16x8 pa1, bf16x8 pa2, bf16x8 pa3) {
;     ...
;     PV_D0(0); PV_D0(1); PV_D0(2); PV_D0(3);
	ds_read_b64_tr_b16 v[248:249], v181 offset:29184
	ds_read_b64_tr_b16 v[250:251], v181 offset:31232
	ds_read_b64_tr_b16 v[98:99], v181 offset:17408
	ds_read_b64_tr_b16 v[100:101], v181 offset:19456
	ds_read_b64_tr_b16 v[102:103], v181 offset:21504
	ds_read_b64_tr_b16 v[104:105], v181 offset:23552
	ds_read_b64_tr_b16 v[106:107], v181 offset:25600
	ds_read_b64_tr_b16 v[108:109], v181 offset:27648
	ds_read_b64_tr_b16 v[110:111], v181 offset:29696
	ds_read_b64_tr_b16 v[112:113], v181 offset:31744
	v_mfma_f32_32x32x16_bf16 v[66:81], v[82:85], v[220:223], v[66:81]
	ds_read_b64_tr_b16 v[220:221], v181 offset:17920
	ds_read_b64_tr_b16 v[222:223], v181 offset:19968
	v_mfma_f32_32x32x16_bf16 v[66:81], v[86:89], v[224:227], v[66:81]
	ds_read_b64_tr_b16 v[224:225], v181 offset:22016
	ds_read_b64_tr_b16 v[226:227], v181 offset:24064
	v_mfma_f32_32x32x16_bf16 v[66:81], v[90:93], v[228:231], v[66:81]
	s_waitcnt lgkmcnt(13)
	ds_read_b64_tr_b16 v[228:229], v181 offset:26112
	ds_read_b64_tr_b16 v[230:231], v181 offset:28160
	v_mfma_f32_32x32x16_bf16 v[66:81], v[94:97], v[232:235], v[66:81]
	s_waitcnt lgkmcnt(13)
	ds_read_b64_tr_b16 v[232:233], v181 offset:30208
	ds_read_b64_tr_b16 v[234:235], v181 offset:32256
	v_mfma_f32_32x32x16_bf16 v[50:65], v[82:85], v[236:239], v[50:65]
	v_mfma_f32_32x32x16_bf16 v[50:65], v[86:89], v[240:243], v[50:65]
	s_waitcnt lgkmcnt(15)
	v_mfma_f32_32x32x16_bf16 v[50:65], v[90:93], v[244:247], v[50:65]
	v_mfma_f32_32x32x16_bf16 v[50:65], v[94:97], v[248:251], v[50:65]
	s_waitcnt lgkmcnt(12)
	v_mfma_f32_32x32x16_bf16 v[34:49], v[82:85], v[98:101], v[34:49]
	v_mfma_f32_32x32x16_bf16 v[34:49], v[86:89], v[102:105], v[34:49]
	s_waitcnt lgkmcnt(8)
	v_mfma_f32_32x32x16_bf16 v[34:49], v[90:93], v[106:109], v[34:49]
	v_mfma_f32_32x32x16_bf16 v[34:49], v[94:97], v[110:113], v[34:49]
	s_waitcnt lgkmcnt(6)
	v_mfma_f32_32x32x16_bf16 v[18:33], v[82:85], v[220:223], v[18:33]
	v_cndmask_b32_e64 v82, 0, 1, s[66:67]
	v_cmp_ne_u32_e64 s[4:5], 1, v82
	s_andn2_b64 vcc, exec, s[66:67]
	s_waitcnt lgkmcnt(4)
	v_mfma_f32_32x32x16_bf16 v[18:33], v[86:89], v[224:227], v[18:33]
	s_waitcnt lgkmcnt(0)
	v_mfma_f32_32x32x16_bf16 v[18:33], v[90:93], v[228:231], v[18:33]
	v_mfma_f32_32x32x16_bf16 v[18:33], v[94:97], v[232:235], v[18:33]
	s_cbranch_vccnz .LBB0_811
	s_waitcnt vmcnt(3)
	ds_write_b128 v192, v[8:11] offset:49152
	s_waitcnt vmcnt(1)
	ds_write_b128 v192, v[162:165] offset:61440
	s_waitcnt vmcnt(0)
	ds_write_b128 v193, v[166:169] offset:49408
	ds_write_b128 v194, v[4:7]
	ds_write_b128 v195, v[12:15]

; __device__ __forceinline__ void mask_tile(f32x16& p0, f32x16& p1, int dq) {
;     const float NEG = -__builtin_inff();
; #pragma unroll
;     for (int r = 0; r < 16; ++r) {
;         const int c = (r & 3) + 8 * (r >> 2);
;         if (dq - c < 0) p0[r] = NEG;
;         if (dq - c - 32 < 0) p1[r] = NEG;
;     }
; }
; template <int DQK, int KB>
; __device__ __forceinline__ void qkt(f32x16& p0, f32x16& p1, const char* K_lds, int r32, int hi, const bf16x8* qr) {
;     constexpr int ROWB = DQK * 2, SHM_K = 64 * ROWB;
;     p0 = f32x16{}; p1 = f32x16{};
;     const char* kb[4];
; #pragma unroll
;     for (int dd = 0; dd < 4; ++dd) kb[dd] = K_lds + KB * SHM_K + r32 * ROWB + (((dd * 16 + hi * 8) * 2) ^ ((r32 & 7) << 4));
; #pragma unroll
;     for (int d0 = 0; d0 < DQK / 16; ++d0) { const char* a = kb[d0 & 3] + (d0 >> 2) * 128;
;         bf16x8 b0 = *reinterpret_cast<const bf16x8*>(a);
;         bf16x8 b1 = *reinterpret_cast<const bf16x8*>(a + 32 * ROWB);
;         p0 = __builtin_amdgcn_mfma_f32_32x32x16_bf16(b0, qr[d0], p0, 0, 0, 0);
;         p1 = __builtin_amdgcn_mfma_f32_32x32x16_bf16(b1, qr[d0], p1, 0, 0, 0); }
.LBB0_813:
	v_add_u32_e32 v219, v189, v183
	v_add_u32_e32 v224, v189, v184
	v_add_u32_e32 v225, v189, v185
	v_add_u32_e32 v226, v189, v186
	ds_read_b128 v[98:101], v219
	ds_read_b128 v[82:85], v219 offset:12288
	ds_read_b128 v[220:223], v224
	ds_read_b128 v[228:231], v224 offset:12288
	ds_read_b128 v[232:235], v225
	ds_read_b128 v[236:239], v225 offset:12288
	ds_read_b128 v[240:243], v226
	ds_read_b128 v[244:247], v226 offset:12288
	ds_read_b128 v[248:251], v219 offset:128
	s_waitcnt lgkmcnt(7)
	v_mfma_f32_32x32x16_bf16 v[98:113], v[98:101], v[158:161], 0
	v_mfma_f32_32x32x16_bf16 v[82:97], v[82:85], v[158:161], 0
	s_waitcnt lgkmcnt(5)
	v_mfma_f32_32x32x16_bf16 v[98:113], v[220:223], v[154:157], v[98:113]
	ds_read_b128 v[220:223], v219 offset:12416
	v_mfma_f32_32x32x16_bf16 v[82:97], v[228:231], v[154:157], v[82:97]
	ds_read_b128 v[228:231], v224 offset:128
	s_waitcnt lgkmcnt(5)
	v_mfma_f32_32x32x16_bf16 v[98:113], v[232:235], v[150:153], v[98:113]
	ds_read_b128 v[232:235], v224 offset:12416
	v_mfma_f32_32x32x16_bf16 v[82:97], v[236:239], v[150:153], v[82:97]
	ds_read_b128 v[236:239], v225 offset:128
	s_waitcnt lgkmcnt(5)
	v_mfma_f32_32x32x16_bf16 v[98:113], v[240:243], v[142:145], v[98:113]
	ds_read_b128 v[240:243], v225 offset:12416
	v_mfma_f32_32x32x16_bf16 v[82:97], v[244:247], v[142:145], v[82:97]
	ds_read_b128 v[244:247], v226 offset:128
	s_waitcnt lgkmcnt(5)
	v_mfma_f32_32x32x16_bf16 v[98:113], v[248:251], v[138:141], v[98:113]
	ds_read_b128 v[248:251], v226 offset:12416
	v_mfma_f32_32x32x16_bf16 v[82:97], v[220:223], v[138:141], v[82:97]
	ds_read_b128 v[220:223], v219 offset:256
	s_waitcnt lgkmcnt(5)
	v_mfma_f32_32x32x16_bf16 v[98:113], v[228:231], v[134:137], v[98:113]
	ds_read_b128 v[228:231], v219 offset:12544
	v_mfma_f32_32x32x16_bf16 v[82:97], v[232:235], v[134:137], v[82:97]
	ds_read_b128 v[232:235], v224 offset:256
	s_waitcnt lgkmcnt(5)
	v_mfma_f32_32x32x16_bf16 v[98:113], v[236:239], v[130:133], v[98:113]
	ds_read_b128 v[236:239], v224 offset:12544
	v_mfma_f32_32x32x16_bf16 v[82:97], v[240:243], v[130:133], v[82:97]
	ds_read_b128 v[240:243], v225 offset:256
	s_waitcnt lgkmcnt(5)
	v_mfma_f32_32x32x16_bf16 v[98:113], v[244:247], v[126:129], v[98:113]
	ds_read_b128 v[244:247], v225 offset:12544
	v_mfma_f32_32x32x16_bf16 v[82:97], v[248:251], v[126:129], v[82:97]
	ds_read_b128 v[248:251], v226 offset:256
	s_waitcnt lgkmcnt(5)
	v_mfma_f32_32x32x16_bf16 v[98:113], v[220:223], v[122:125], v[98:113]
	ds_read_b128 v[220:223], v226 offset:12544
	v_mfma_f32_32x32x16_bf16 v[82:97], v[228:231], v[122:125], v[82:97]
	s_waitcnt lgkmcnt(4)
	v_mfma_f32_32x32x16_bf16 v[98:113], v[232:235], v[118:121], v[98:113]
	v_mfma_f32_32x32x16_bf16 v[82:97], v[236:239], v[118:121], v[82:97]
	s_waitcnt lgkmcnt(2)
	v_mfma_f32_32x32x16_bf16 v[98:113], v[240:243], v[114:117], v[98:113]
	v_mfma_f32_32x32x16_bf16 v[82:97], v[244:247], v[114:117], v[82:97]
	s_add_i32 s6, s78, 0xffffffbf
	s_cmp_le_i32 s6, s84
	s_waitcnt lgkmcnt(1)
	v_mfma_f32_32x32x16_bf16 v[98:113], v[248:251], v[146:149], v[98:113]
	s_waitcnt lgkmcnt(0)
	v_mfma_f32_32x32x16_bf16 v[82:97], v[220:223], v[146:149], v[82:97]
	s_cbranch_scc1 .LBB0_815
	v_add_u32_e32 v219, 0xffffff80, v206
	v_cmp_gt_i32_e64 s[64:65], 26, v219
	v_cmp_gt_i32_e64 s[66:67], 27, v219
	v_cmp_gt_i32_e64 s[62:63], 25, v219
	s_and_b64 s[64:65], s[66:67], s[64:65]
	v_cmp_gt_i32_e64 s[60:61], 24, v219
	s_and_b64 s[62:63], s[64:65], s[62:63]
	v_cmp_gt_i32_e64 s[58:59], 19, v219
	s_and_b64 s[60:61], s[62:63], s[60:61]
	v_cmp_gt_i32_e64 s[56:57], 18, v219
	s_and_b64 s[58:59], s[60:61], s[58:59]
	v_cmp_gt_i32_e64 s[54:55], 17, v219
	s_and_b64 s[56:57], s[58:59], s[56:57]
	v_cmp_gt_i32_e64 s[52:53], 16, v219
	s_and_b64 s[54:55], s[56:57], s[54:55]
	v_cmp_gt_i32_e64 s[50:51], 11, v219
	s_and_b64 s[52:53], s[54:55], s[52:53]
	v_cmp_gt_i32_e64 s[48:49], 10, v219
	s_and_b64 s[50:51], s[52:53], s[50:51]
	v_cmp_gt_i32_e64 s[46:47], 9, v219
	s_and_b64 s[48:49], s[50:51], s[48:49]
	v_cmp_gt_i32_e64 s[44:45], 8, v219
	s_and_b64 s[46:47], s[48:49], s[46:47]
	v_cmp_gt_i32_e64 s[42:43], 3, v219
	s_and_b64 s[44:45], s[46:47], s[44:45]
	v_cmp_gt_i32_e64 s[40:41], 2, v219
	s_and_b64 s[42:43], s[44:45], s[42:43]
	v_cmp_gt_i32_e64 s[38:39], 1, v219
	s_and_b64 s[40:41], s[42:43], s[40:41]
	v_cmp_gt_i32_e64 s[36:37], 0, v219
	s_and_b64 s[38:39], s[40:41], s[38:39]
	s_and_b64 s[36:37], s[38:39], s[36:37]
	v_cmp_gt_i32_e64 s[34:35], 58, v219
	v_cndmask_b32_e64 v98, v98, v198, s[36:37]
	v_cmp_gt_i32_e64 s[36:37], 59, v219
	v_cmp_gt_i32_e64 s[30:31], 57, v219
	s_and_b64 s[34:35], s[36:37], s[34:35]
	v_cmp_gt_i32_e64 s[28:29], 56, v219
	s_and_b64 s[30:31], s[34:35], s[30:31]
	v_cmp_gt_i32_e64 s[26:27], 51, v219
	s_and_b64 s[28:29], s[30:31], s[28:29]
	v_cmp_gt_i32_e64 s[24:25], 50, v219
	s_and_b64 s[26:27], s[28:29], s[26:27]
	v_cmp_gt_i32_e64 s[22:23], 49, v219
	s_and_b64 s[24:25], s[26:27], s[24:25]
	v_cmp_gt_i32_e64 s[20:21], 48, v219
	s_and_b64 s[22:23], s[24:25], s[22:23]
	v_cmp_gt_i32_e64 s[18:19], 43, v219
	s_and_b64 s[20:21], s[22:23], s[20:21]
	v_cmp_gt_i32_e64 s[16:17], 42, v219
	s_and_b64 s[18:19], s[20:21], s[18:19]
	v_cmp_gt_i32_e64 s[14:15], 41, v219
	s_and_b64 s[16:17], s[18:19], s[16:17]
	v_cmp_gt_i32_e64 s[12:13], 40, v219
	s_and_b64 s[14:15], s[16:17], s[14:15]
	v_cmp_gt_i32_e64 s[10:11], 35, v219
	s_and_b64 s[12:13], s[14:15], s[12:13]
	v_cmp_gt_i32_e64 s[8:9], 34, v219
	s_and_b64 s[10:11], s[12:13], s[10:11]
	v_cmp_gt_i32_e64 s[6:7], 33, v219
	s_and_b64 s[8:9], s[10:11], s[8:9]
	v_cmp_gt_i32_e32 vcc, 32, v219
	s_and_b64 s[6:7], s[8:9], s[6:7]
	s_and_b64 vcc, s[6:7], vcc
	v_cndmask_b32_e64 v113, v113, v198, s[66:67]
	v_cndmask_b32_e64 v112, v112, v198, s[64:65]
	v_cndmask_b32_e64 v111, v111, v198, s[62:63]
	v_cndmask_b32_e64 v110, v110, v198, s[60:61]
	v_cndmask_b32_e64 v109, v109, v198, s[58:59]
	v_cndmask_b32_e64 v108, v108, v198, s[56:57]
	v_cndmask_b32_e64 v107, v107, v198, s[54:55]
	v_cndmask_b32_e64 v106, v106, v198, s[52:53]
	v_cndmask_b32_e64 v105, v105, v198, s[50:51]
	v_cndmask_b32_e64 v104, v104, v198, s[48:49]
	v_cndmask_b32_e64 v103, v103, v198, s[46:47]
	v_cndmask_b32_e64 v102, v102, v198, s[44:45]
	v_cndmask_b32_e64 v101, v101, v198, s[42:43]
	v_cndmask_b32_e64 v100, v100, v198, s[40:41]
	v_cndmask_b32_e64 v99, v99, v198, s[38:39]
	v_cndmask_b32_e64 v97, v97, v198, s[36:37]
	v_cndmask_b32_e64 v96, v96, v198, s[34:35]
	v_cndmask_b32_e64 v95, v95, v198, s[30:31]
	v_cndmask_b32_e64 v94, v94, v198, s[28:29]
	v_cndmask_b32_e64 v93, v93, v198, s[26:27]
	v_cndmask_b32_e64 v92, v92, v198, s[24:25]
	v_cndmask_b32_e64 v91, v91, v198, s[22:23]
	v_cndmask_b32_e64 v90, v90, v198, s[20:21]
	v_cndmask_b32_e64 v89, v89, v198, s[18:19]
	v_cndmask_b32_e64 v88, v88, v198, s[16:17]
	v_cndmask_b32_e64 v87, v87, v198, s[14:15]
	v_cndmask_b32_e64 v86, v86, v198, s[12:13]
	v_cndmask_b32_e64 v85, v85, v198, s[10:11]
	v_cndmask_b32_e64 v84, v84, v198, s[8:9]
	v_cndmask_b32_e64 v83, v83, v198, s[6:7]
	v_cndmask_b32_e32 v82, v82, v198, vcc

; template <int DQK> __device__ __forceinline__ void partialSM(f32x16& p0, f32x16& p1, float& m_reg, float& mn, float& alpha) {
;     ...
;     mn = need ? fmaxf(m_reg, pmax) : m_reg; alpha = need ? __builtin_amdgcn_exp2f((m_reg - mn) * C2) : 1.f; m_reg = mn;
;     const float mnL = -mn * C2;
; #pragma unroll
;     for (int r = 0; r < 16; ++r) p0[r] = fmaf(p0[r], C2, mnL);
; #pragma unroll
;     for (int r = 0; r < 16; ++r) p1[r] = fmaf(p1[r], C2, mnL);
; #pragma unroll
;     for (int r = 0; r < 16; ++r) p0[r] = __builtin_amdgcn_exp2f(p0[r]);
; }
; __device__ __forceinline__ void finishSM(f32x16& p0, f32x16& p1, float alpha, float& l_reg, bf16x8& pa0, bf16x8& pa1, bf16x8& pa2, bf16x8& pa3) {
; #pragma unroll
;     for (int r = 0; r < 16; ++r) p1[r] = __builtin_amdgcn_exp2f(p1[r]);
;     float ps = 0;
; #pragma unroll
;     for (int r = 0; r < 16; ++r) ps += p0[r];
; #pragma unroll
;     for (int r = 0; r < 16; ++r) ps += p1[r];
;     { auto rr = __builtin_amdgcn_permlane32_swap(__float_as_uint(ps), __float_as_uint(ps), false, false);
;       ps = __uint_as_float(rr[0]) + __uint_as_float(rr[1]); }
;     l_reg = l_reg * alpha + ps;
;     ...
;     PK4(p0, 0, pa0); PK4(p0, 8, pa1); PK4(p1, 0, pa2); PK4(p1, 8, pa3);
.LBB0_819:
	ds_read_b64_tr_b16 v[236:237], v181 offset:32768
	ds_read_b64_tr_b16 v[238:239], v181 offset:34816
	ds_read_b64_tr_b16 v[240:241], v181 offset:36864
	ds_read_b64_tr_b16 v[242:243], v181 offset:38912
	ds_read_b64_tr_b16 v[244:245], v181 offset:40960
	ds_read_b64_tr_b16 v[246:247], v181 offset:43008
	ds_read_b64_tr_b16 v[248:249], v181 offset:45056
	ds_read_b64_tr_b16 v[250:251], v181 offset:47104
	v_cndmask_b32_e64 v216, v216, v220, s[6:7]
	v_mul_f32_e32 v220, 0xbdd53b94, v216
	v_fmamk_f32 v98, v98, 0x3dd53b94, v220
	v_fmamk_f32 v99, v99, 0x3dd53b94, v220
	v_fmamk_f32 v100, v100, 0x3dd53b94, v220
	v_fmamk_f32 v101, v101, 0x3dd53b94, v220
	v_fmamk_f32 v102, v102, 0x3dd53b94, v220
	v_fmamk_f32 v103, v103, 0x3dd53b94, v220
	v_fmamk_f32 v104, v104, 0x3dd53b94, v220
	v_fmamk_f32 v105, v105, 0x3dd53b94, v220
	v_fmamk_f32 v106, v106, 0x3dd53b94, v220
	v_fmamk_f32 v107, v107, 0x3dd53b94, v220
	v_fmamk_f32 v108, v108, 0x3dd53b94, v220
	v_fmamk_f32 v109, v109, 0x3dd53b94, v220
	v_fmamk_f32 v110, v110, 0x3dd53b94, v220
	v_fmamk_f32 v111, v111, 0x3dd53b94, v220
	v_fmamk_f32 v112, v112, 0x3dd53b94, v220
	v_fmamk_f32 v113, v113, 0x3dd53b94, v220
	v_fmamk_f32 v82, v82, 0x3dd53b94, v220
	v_fmamk_f32 v83, v83, 0x3dd53b94, v220
	v_fmamk_f32 v84, v84, 0x3dd53b94, v220
	v_fmamk_f32 v85, v85, 0x3dd53b94, v220
	v_fmamk_f32 v86, v86, 0x3dd53b94, v220
	v_fmamk_f32 v87, v87, 0x3dd53b94, v220
	v_fmamk_f32 v88, v88, 0x3dd53b94, v220
	v_fmamk_f32 v89, v89, 0x3dd53b94, v220
	v_fmamk_f32 v90, v90, 0x3dd53b94, v220
	v_fmamk_f32 v91, v91, 0x3dd53b94, v220
	v_fmamk_f32 v92, v92, 0x3dd53b94, v220
	v_fmamk_f32 v93, v93, 0x3dd53b94, v220
	v_fmamk_f32 v94, v94, 0x3dd53b94, v220
	v_fmamk_f32 v95, v95, 0x3dd53b94, v220
	v_fmamk_f32 v96, v96, 0x3dd53b94, v220
	v_fmac_f32_e32 v220, 0x3dd53b94, v97
	v_exp_f32_e32 v97, v98
	v_exp_f32_e32 v98, v99
	v_exp_f32_e32 v99, v100
	v_exp_f32_e32 v100, v101
	v_exp_f32_e32 v101, v102
	v_exp_f32_e32 v102, v103
	v_exp_f32_e32 v103, v104
	v_exp_f32_e32 v104, v105
	v_exp_f32_e32 v105, v106
	v_exp_f32_e32 v106, v107
	v_exp_f32_e32 v107, v108
	v_exp_f32_e32 v108, v109
	v_exp_f32_e32 v109, v110
	v_exp_f32_e32 v110, v111
	v_exp_f32_e32 v111, v112
	v_exp_f32_e32 v112, v113
	v_exp_f32_e32 v113, v82
	v_add_f32_e32 v82, 0, v97
	v_add_f32_e32 v82, v98, v82
	v_add_f32_e32 v82, v99, v82
	v_add_f32_e32 v82, v100, v82
	v_add_f32_e32 v82, v101, v82
	v_add_f32_e32 v82, v102, v82
	v_add_f32_e32 v82, v103, v82
	v_add_f32_e32 v82, v104, v82
	v_add_f32_e32 v82, v105, v82
	v_add_f32_e32 v82, v106, v82
	v_add_f32_e32 v82, v107, v82
	v_add_f32_e32 v82, v108, v82
	v_add_f32_e32 v82, v109, v82
	v_exp_f32_e32 v221, v83
	v_add_f32_e32 v82, v110, v82
	v_exp_f32_e32 v222, v84
	v_add_f32_e32 v82, v111, v82
	v_exp_f32_e32 v223, v85
	v_add_f32_e32 v82, v112, v82
	v_exp_f32_e32 v224, v86
	v_add_f32_e32 v82, v113, v82
	v_exp_f32_e32 v225, v87
	v_add_f32_e32 v82, v221, v82
	v_exp_f32_e32 v226, v88
	v_add_f32_e32 v82, v222, v82
	v_exp_f32_e32 v227, v89
	v_add_f32_e32 v82, v223, v82
	v_exp_f32_e32 v228, v90
	v_add_f32_e32 v82, v224, v82
	v_exp_f32_e32 v229, v91
	v_add_f32_e32 v82, v225, v82
	v_exp_f32_e32 v230, v92
	v_add_f32_e32 v82, v226, v82
	v_exp_f32_e32 v231, v93
	v_add_f32_e32 v82, v227, v82
	v_exp_f32_e32 v232, v94
	v_add_f32_e32 v82, v228, v82
	v_exp_f32_e32 v233, v95
	v_add_f32_e32 v82, v229, v82
	v_exp_f32_e32 v234, v96
	v_add_f32_e32 v82, v230, v82
	v_exp_f32_e32 v220, v220
	v_add_f32_e32 v82, v231, v82
	v_add_f32_e32 v82, v232, v82
	v_add_f32_e32 v82, v233, v82
	v_add_f32_e32 v82, v234, v82
	v_add_f32_e32 v82, v220, v82
	v_mov_b32_e32 v83, v82
	s_nop 1
	v_permlane32_swap_b32_e32 v82, v83
	v_cvt_pk_bf16_f32 v84, v97, v98
	v_cvt_pk_bf16_f32 v85, v99, v100
	v_cvt_pk_bf16_f32 v86, v101, v102
	v_cvt_pk_bf16_f32 v87, v103, v104
	v_cvt_pk_bf16_f32 v88, v105, v106
	v_cvt_pk_bf16_f32 v89, v107, v108
	v_cvt_pk_bf16_f32 v90, v109, v110
	v_cvt_pk_bf16_f32 v91, v111, v112
	v_cvt_pk_bf16_f32 v92, v113, v221
	v_cvt_pk_bf16_f32 v93, v222, v223
	v_cvt_pk_bf16_f32 v94, v224, v225
	v_cvt_pk_bf16_f32 v95, v226, v227
	v_cvt_pk_bf16_f32 v96, v228, v229
	v_cvt_pk_bf16_f32 v97, v230, v231
	v_cvt_pk_bf16_f32 v98, v232, v233
	v_cvt_pk_bf16_f32 v99, v234, v220
	s_nop 0
	v_permlane32_swap_b32_e32 v84, v86
	v_permlane32_swap_b32_e32 v85, v87
	v_permlane32_swap_b32_e32 v88, v90
	v_permlane32_swap_b32_e32 v89, v91
	v_permlane32_swap_b32_e32 v92, v94
	v_permlane32_swap_b32_e32 v93, v95
	v_permlane32_swap_b32_e32 v96, v98
	v_permlane32_swap_b32_e32 v97, v99
	s_waitcnt lgkmcnt(0)
; template <int VB>
; __device__ __forceinline__ void pv_tile(f32x16* o, int vb0, bf16x8 pa0, bf16x8 pa1, bf16x8 pa2, bf16x8 pa3) {
;     ...
;     PV_D0(0); PV_D0(1); PV_D0(2); PV_D0(3);
	ds_read_b64_tr_b16 v[220:221], v181 offset:33280
	ds_read_b64_tr_b16 v[222:223], v181 offset:35328
	ds_read_b64_tr_b16 v[224:225], v181 offset:37376
	ds_read_b64_tr_b16 v[226:227], v181 offset:39424
	ds_read_b64_tr_b16 v[228:229], v181 offset:41472
	ds_read_b64_tr_b16 v[230:231], v181 offset:43520
	ds_read_b64_tr_b16 v[232:233], v181 offset:45568
	ds_read_b64_tr_b16 v[234:235], v181 offset:47616
	ds_read_b64_tr_b16 v[100:101], v181 offset:33792
	ds_read_b64_tr_b16 v[102:103], v181 offset:35840
	ds_read_b64_tr_b16 v[104:105], v181 offset:37888
	ds_read_b64_tr_b16 v[106:107], v181 offset:39936
	ds_read_b64_tr_b16 v[108:109], v181 offset:41984
	ds_read_b64_tr_b16 v[110:111], v181 offset:44032
	v_mfma_f32_32x32x16_bf16 v[66:81], v[84:87], v[236:239], v[66:81]
	s_waitcnt lgkmcnt(13)
	ds_read_b64_tr_b16 v[236:237], v181 offset:46080
	ds_read_b64_tr_b16 v[238:239], v181 offset:48128
	v_mfma_f32_32x32x16_bf16 v[66:81], v[88:91], v[240:243], v[66:81]
	s_waitcnt lgkmcnt(13)
	ds_read_b64_tr_b16 v[240:241], v181 offset:34304
	ds_read_b64_tr_b16 v[242:243], v181 offset:36352
	v_mfma_f32_32x32x16_bf16 v[66:81], v[92:95], v[244:247], v[66:81]
	s_waitcnt lgkmcnt(13)
	ds_read_b64_tr_b16 v[244:245], v181 offset:38400
	ds_read_b64_tr_b16 v[246:247], v181 offset:40448
	v_mfma_f32_32x32x16_bf16 v[66:81], v[96:99], v[248:251], v[66:81]
	s_waitcnt lgkmcnt(13)
	ds_read_b64_tr_b16 v[248:249], v181 offset:42496
	ds_read_b64_tr_b16 v[250:251], v181 offset:44544
	s_waitcnt lgkmcnt(15)
	v_mfma_f32_32x32x16_bf16 v[50:65], v[84:87], v[220:223], v[50:65]
	s_waitcnt lgkmcnt(13)
	ds_read_b64_tr_b16 v[220:221], v181 offset:46592
	ds_read_b64_tr_b16 v[222:223], v181 offset:48640
	v_mfma_f32_32x32x16_bf16 v[50:65], v[88:91], v[224:227], v[50:65]
	s_waitcnt lgkmcnt(15)
	v_mfma_f32_32x32x16_bf16 v[50:65], v[92:95], v[228:231], v[50:65]
	v_mfma_f32_32x32x16_bf16 v[50:65], v[96:99], v[232:235], v[50:65]
	s_waitcnt lgkmcnt(12)
	v_mfma_f32_32x32x16_bf16 v[34:49], v[84:87], v[100:103], v[34:49]
	v_mfma_f32_32x32x16_bf16 v[34:49], v[88:91], v[104:107], v[34:49]
	s_waitcnt lgkmcnt(8)
	v_mfma_f32_32x32x16_bf16 v[34:49], v[92:95], v[108:111], v[34:49]
	v_mfma_f32_32x32x16_bf16 v[34:49], v[96:99], v[236:239], v[34:49]
	s_waitcnt lgkmcnt(6)
	v_mfma_f32_32x32x16_bf16 v[18:33], v[84:87], v[240:243], v[18:33]
	s_andn2_b64 vcc, exec, s[80:81]
	s_waitcnt lgkmcnt(4)
	v_mfma_f32_32x32x16_bf16 v[18:33], v[88:91], v[244:247], v[18:33]
	s_waitcnt lgkmcnt(0)
	v_mfma_f32_32x32x16_bf16 v[18:33], v[92:95], v[248:251], v[18:33]
	v_mfma_f32_32x32x16_bf16 v[18:33], v[96:99], v[220:223], v[18:33]
	s_cbranch_vccnz .LBB0_794
	s_waitcnt vmcnt(3)
	ds_write_b128 v196, v[8:11]
	s_waitcnt vmcnt(1)
	ds_write_b128 v196, v[162:165] offset:12288
	s_waitcnt vmcnt(0)
	ds_write_b128 v197, v[166:169]
	ds_write_b128 v194, v[4:7] offset:16384
	ds_write_b128 v195, v[12:15] offset:16384
	s_branch .LBB0_794
